# U and V gather addresses by one v_mad_u32_u16 (id*128 + lane offset) instead of sdwa shift + or
# baseline (speedup 1.0000x reference)
.LBB0_1048:
	s_cmp_lt_i32 s40, 11
	s_cselect_b64 s[2:3], -1, 0
	s_cmp_gt_i32 s41, 10
	s_cselect_b64 s[4:5], -1, 0
	s_and_b64 s[10:11], s[2:3], s[4:5]
	s_andn2_b64 vcc, exec, s[10:11]
	s_cbranch_vccnz .LBB0_1075
	s_mov_b64 s[2:3], s[0:1]
	s_waitcnt vmcnt(0) lgkmcnt(0)
	v_mbcnt_lo_u32_b32 v0, -1, 0
	v_mbcnt_hi_u32_b32 v0, -1, v0
	s_load_dwordx2 s[4:5], s[2:3], 0xb8
	v_and_b32_e32 v9, 7, v0
	v_lshrrev_b32_e32 v10, 3, v0
	v_lshlrev_b32_e32 v1, 4, v9
	v_lshlrev_b32_e32 v2, 5, v10
	v_lshlrev_b32_e32 v3, 2, v0
	v_lshlrev_b32_e32 v4, 5, v9
	v_and_b32_e32 v12, 2, v0
	v_cmp_ne_u32_e64 s[44:45], 0, v12
	v_and_b32_e32 v12, 1, v0
	v_cmp_ne_u32_e64 s[42:43], 0, v12
	v_mov_b32_e32 v5, 0
	v_mov_b32_e32 v7, -1
	s_mov_b32 s47, 7
	s_movk_i32 s46, 0x80
	s_mov_b32 s38, 0x200000
	s_mov_b32 s39, 0x20000
	s_lshl_b32 s16, s24, 1
	s_and_b32 s16, s16, 14
	s_mov_b32 s17, 0
	s_waitcnt lgkmcnt(0)
	s_add_u32 s28, s4, 0x18800000
	s_addc_u32 s29, s5, 0

.Lub_got_p1:
	s_mov_b32 s21, s22
	s_mov_b32 s49, s50
	s_cmp_eq_u32 s48, 0
	s_cbranch_scc1 .Lub_next_slice
	s_lshl_b32 s2, s20, 8
	s_add_u32 s2, s28, s2
	s_addc_u32 s3, s29, 0
	global_load_dwordx4 v[8:11], v2, s[2:3]
	global_load_dwordx4 v[12:15], v2, s[2:3] offset:16
	s_lshl_b32 s2, s20, 12
	s_add_u32 s2, s30, s2
	s_addc_u32 s3, s31, 0
	global_load_dwordx4 v[24:27], v4, s[2:3]
	global_load_dwordx4 v[28:31], v4, s[2:3] offset:16
	s_lshl_b32 s2, s21, 8
	s_add_u32 s2, s28, s2
	s_addc_u32 s3, s29, 0
	global_load_dwordx4 v[16:19], v2, s[2:3]
	global_load_dwordx4 v[20:23], v2, s[2:3] offset:16
	s_waitcnt vmcnt(0)
	v_mad_u32_u16 v112, v8, s46, v1
	buffer_load_dwordx4 v[48:51], v112, s[36:39], 0 offen
	v_mad_u32_u16 v113, v8, s46, v1 op_sel:[1,0,0,0]
	buffer_load_dwordx4 v[52:55], v113, s[36:39], 0 offen
	v_mad_u32_u16 v112, v9, s46, v1
	buffer_load_dwordx4 v[56:59], v112, s[36:39], 0 offen
	v_mad_u32_u16 v113, v9, s46, v1 op_sel:[1,0,0,0]
	buffer_load_dwordx4 v[60:63], v113, s[36:39], 0 offen
	v_mad_u32_u16 v112, v10, s46, v1
	buffer_load_dwordx4 v[64:67], v112, s[36:39], 0 offen
	v_mad_u32_u16 v113, v10, s46, v1 op_sel:[1,0,0,0]
	buffer_load_dwordx4 v[68:71], v113, s[36:39], 0 offen
	v_mad_u32_u16 v112, v11, s46, v1
	buffer_load_dwordx4 v[72:75], v112, s[36:39], 0 offen
	v_mad_u32_u16 v113, v11, s46, v1 op_sel:[1,0,0,0]
	buffer_load_dwordx4 v[76:79], v113, s[36:39], 0 offen
	v_mad_u32_u16 v112, v12, s46, v1
	buffer_load_dwordx4 v[80:83], v112, s[36:39], 0 offen
	v_mad_u32_u16 v113, v12, s46, v1 op_sel:[1,0,0,0]
	buffer_load_dwordx4 v[84:87], v113, s[36:39], 0 offen
	v_mad_u32_u16 v112, v13, s46, v1
	buffer_load_dwordx4 v[88:91], v112, s[36:39], 0 offen
	v_mad_u32_u16 v113, v13, s46, v1 op_sel:[1,0,0,0]
	buffer_load_dwordx4 v[92:95], v113, s[36:39], 0 offen
	v_mad_u32_u16 v112, v14, s46, v1
	buffer_load_dwordx4 v[96:99], v112, s[36:39], 0 offen
	v_mad_u32_u16 v113, v14, s46, v1 op_sel:[1,0,0,0]
	buffer_load_dwordx4 v[100:103], v113, s[36:39], 0 offen
	v_mad_u32_u16 v112, v15, s46, v1
	buffer_load_dwordx4 v[104:107], v112, s[36:39], 0 offen
	v_mad_u32_u16 v113, v15, s46, v1 op_sel:[1,0,0,0]
	buffer_load_dwordx4 v[108:111], v113, s[36:39], 0 offen
	global_load_dword v252, v5, s[28:29]

.Lub_got_l0:
	s_lshl_b32 s2, s22, 8
	s_add_u32 s2, s28, s2
	s_addc_u32 s3, s29, 0
	global_load_dwordx4 v[8:11], v2, s[2:3]
	global_load_dwordx4 v[12:15], v2, s[2:3] offset:16
	s_lshl_b32 s2, s21, 12
	s_add_u32 s2, s30, s2
	s_addc_u32 s3, s31, 0
	global_load_dwordx4 v[32:35], v4, s[2:3]
	global_load_dwordx4 v[36:39], v4, s[2:3] offset:16
	s_waitcnt vmcnt(20)
	v_cvt_pk_f32_fp8_e32 v[116:117], v48
	v_cvt_pk_f32_fp8_sdwa v[118:119], v48 src0_sel:WORD_1
	v_cvt_pk_f32_fp8_e32 v[120:121], v49
	v_cvt_pk_f32_fp8_sdwa v[122:123], v49 src0_sel:WORD_1
	v_cvt_pk_f32_fp8_e32 v[124:125], v50
	v_cvt_pk_f32_fp8_sdwa v[126:127], v50 src0_sel:WORD_1
	v_cvt_pk_f32_fp8_e32 v[128:129], v51
	v_cvt_pk_f32_fp8_sdwa v[130:131], v51 src0_sel:WORD_1
	v_lshlrev_b32_e32 v148, 16, v24
	v_and_b32_e32 v149, 0xffff0000, v24
	v_lshlrev_b32_e32 v150, 16, v25
	v_and_b32_e32 v151, 0xffff0000, v25
	v_lshlrev_b32_e32 v152, 16, v26
	v_and_b32_e32 v153, 0xffff0000, v26
	v_lshlrev_b32_e32 v154, 16, v27
	v_and_b32_e32 v155, 0xffff0000, v27
	v_lshlrev_b32_e32 v156, 16, v28
	v_and_b32_e32 v157, 0xffff0000, v28
	v_lshlrev_b32_e32 v158, 16, v29
	v_and_b32_e32 v159, 0xffff0000, v29
	v_lshlrev_b32_e32 v160, 16, v30
	v_and_b32_e32 v161, 0xffff0000, v30
	v_lshlrev_b32_e32 v162, 16, v31
	v_and_b32_e32 v163, 0xffff0000, v31
	v_mad_u32_u16 v112, v16, s46, v1
	buffer_load_dwordx4 v[48:51], v112, s[36:39], 0 offen
	v_pk_mul_f32 v[164:165], v[116:117], v[148:149]
	v_pk_fma_f32 v[164:165], v[118:119], v[150:151], v[164:165]
	v_pk_fma_f32 v[164:165], v[120:121], v[152:153], v[164:165]
	v_pk_fma_f32 v[164:165], v[122:123], v[154:155], v[164:165]
	v_pk_fma_f32 v[164:165], v[124:125], v[156:157], v[164:165]
	v_pk_fma_f32 v[164:165], v[126:127], v[158:159], v[164:165]
	v_pk_fma_f32 v[164:165], v[128:129], v[160:161], v[164:165]
	v_pk_fma_f32 v[164:165], v[130:131], v[162:163], v[164:165]
	v_add_f32_e32 v168, v164, v165
	s_waitcnt vmcnt(20)
	v_cvt_pk_f32_fp8_e32 v[132:133], v52
	v_cvt_pk_f32_fp8_sdwa v[134:135], v52 src0_sel:WORD_1
	v_cvt_pk_f32_fp8_e32 v[136:137], v53
	v_cvt_pk_f32_fp8_sdwa v[138:139], v53 src0_sel:WORD_1
	v_cvt_pk_f32_fp8_e32 v[140:141], v54
	v_cvt_pk_f32_fp8_sdwa v[142:143], v54 src0_sel:WORD_1
	v_cvt_pk_f32_fp8_e32 v[144:145], v55
	v_cvt_pk_f32_fp8_sdwa v[146:147], v55 src0_sel:WORD_1
	v_mad_u32_u16 v113, v16, s46, v1 op_sel:[1,0,0,0]
	buffer_load_dwordx4 v[52:55], v113, s[36:39], 0 offen
	v_pk_mul_f32 v[166:167], v[132:133], v[148:149]
	v_pk_fma_f32 v[166:167], v[134:135], v[150:151], v[166:167]
	v_pk_fma_f32 v[166:167], v[136:137], v[152:153], v[166:167]
	v_pk_fma_f32 v[166:167], v[138:139], v[154:155], v[166:167]
	v_pk_fma_f32 v[166:167], v[140:141], v[156:157], v[166:167]
	v_pk_fma_f32 v[166:167], v[142:143], v[158:159], v[166:167]
	v_pk_fma_f32 v[166:167], v[144:145], v[160:161], v[166:167]
	v_pk_fma_f32 v[166:167], v[146:147], v[162:163], v[166:167]
	v_add_f32_e32 v169, v166, v167
	s_waitcnt vmcnt(20)
	v_cvt_pk_f32_fp8_e32 v[116:117], v56
	v_cvt_pk_f32_fp8_sdwa v[118:119], v56 src0_sel:WORD_1
	v_cvt_pk_f32_fp8_e32 v[120:121], v57
	v_cvt_pk_f32_fp8_sdwa v[122:123], v57 src0_sel:WORD_1
	v_cvt_pk_f32_fp8_e32 v[124:125], v58
	v_cvt_pk_f32_fp8_sdwa v[126:127], v58 src0_sel:WORD_1
	v_cvt_pk_f32_fp8_e32 v[128:129], v59
	v_cvt_pk_f32_fp8_sdwa v[130:131], v59 src0_sel:WORD_1
	v_mad_u32_u16 v112, v17, s46, v1
	buffer_load_dwordx4 v[56:59], v112, s[36:39], 0 offen
	v_pk_mul_f32 v[164:165], v[116:117], v[148:149]
	v_pk_fma_f32 v[164:165], v[118:119], v[150:151], v[164:165]
	v_pk_fma_f32 v[164:165], v[120:121], v[152:153], v[164:165]
	v_pk_fma_f32 v[164:165], v[122:123], v[154:155], v[164:165]
	v_pk_fma_f32 v[164:165], v[124:125], v[156:157], v[164:165]
	v_pk_fma_f32 v[164:165], v[126:127], v[158:159], v[164:165]
	v_pk_fma_f32 v[164:165], v[128:129], v[160:161], v[164:165]
	v_pk_fma_f32 v[164:165], v[130:131], v[162:163], v[164:165]
	v_add_f32_e32 v170, v164, v165
	s_waitcnt vmcnt(20)
	v_cvt_pk_f32_fp8_e32 v[132:133], v60
	v_cvt_pk_f32_fp8_sdwa v[134:135], v60 src0_sel:WORD_1
	v_cvt_pk_f32_fp8_e32 v[136:137], v61
	v_cvt_pk_f32_fp8_sdwa v[138:139], v61 src0_sel:WORD_1
	v_cvt_pk_f32_fp8_e32 v[140:141], v62
	v_cvt_pk_f32_fp8_sdwa v[142:143], v62 src0_sel:WORD_1
	v_cvt_pk_f32_fp8_e32 v[144:145], v63
	v_cvt_pk_f32_fp8_sdwa v[146:147], v63 src0_sel:WORD_1
	v_mad_u32_u16 v113, v17, s46, v1 op_sel:[1,0,0,0]
	buffer_load_dwordx4 v[60:63], v113, s[36:39], 0 offen
	v_pk_mul_f32 v[166:167], v[132:133], v[148:149]
	v_pk_fma_f32 v[166:167], v[134:135], v[150:151], v[166:167]
	v_pk_fma_f32 v[166:167], v[136:137], v[152:153], v[166:167]
	v_pk_fma_f32 v[166:167], v[138:139], v[154:155], v[166:167]
	v_pk_fma_f32 v[166:167], v[140:141], v[156:157], v[166:167]
	v_pk_fma_f32 v[166:167], v[142:143], v[158:159], v[166:167]
	v_pk_fma_f32 v[166:167], v[144:145], v[160:161], v[166:167]
	v_pk_fma_f32 v[166:167], v[146:147], v[162:163], v[166:167]
	v_add_f32_e32 v171, v166, v167
	s_waitcnt vmcnt(20)
	v_cvt_pk_f32_fp8_e32 v[116:117], v64
	v_cvt_pk_f32_fp8_sdwa v[118:119], v64 src0_sel:WORD_1
	v_cvt_pk_f32_fp8_e32 v[120:121], v65
	v_cvt_pk_f32_fp8_sdwa v[122:123], v65 src0_sel:WORD_1
	v_cvt_pk_f32_fp8_e32 v[124:125], v66
	v_cvt_pk_f32_fp8_sdwa v[126:127], v66 src0_sel:WORD_1
	v_cvt_pk_f32_fp8_e32 v[128:129], v67
	v_cvt_pk_f32_fp8_sdwa v[130:131], v67 src0_sel:WORD_1
	v_mad_u32_u16 v112, v18, s46, v1
	buffer_load_dwordx4 v[64:67], v112, s[36:39], 0 offen
	v_pk_mul_f32 v[164:165], v[116:117], v[148:149]
	v_pk_fma_f32 v[164:165], v[118:119], v[150:151], v[164:165]
	v_pk_fma_f32 v[164:165], v[120:121], v[152:153], v[164:165]
	v_pk_fma_f32 v[164:165], v[122:123], v[154:155], v[164:165]
	v_pk_fma_f32 v[164:165], v[124:125], v[156:157], v[164:165]
	v_pk_fma_f32 v[164:165], v[126:127], v[158:159], v[164:165]
	v_pk_fma_f32 v[164:165], v[128:129], v[160:161], v[164:165]
	v_pk_fma_f32 v[164:165], v[130:131], v[162:163], v[164:165]
	v_add_f32_e32 v172, v164, v165
	s_waitcnt vmcnt(20)
	v_cvt_pk_f32_fp8_e32 v[132:133], v68
	v_cvt_pk_f32_fp8_sdwa v[134:135], v68 src0_sel:WORD_1
	v_cvt_pk_f32_fp8_e32 v[136:137], v69
	v_cvt_pk_f32_fp8_sdwa v[138:139], v69 src0_sel:WORD_1
	v_cvt_pk_f32_fp8_e32 v[140:141], v70
	v_cvt_pk_f32_fp8_sdwa v[142:143], v70 src0_sel:WORD_1
	v_cvt_pk_f32_fp8_e32 v[144:145], v71
	v_cvt_pk_f32_fp8_sdwa v[146:147], v71 src0_sel:WORD_1
	v_mad_u32_u16 v113, v18, s46, v1 op_sel:[1,0,0,0]
	buffer_load_dwordx4 v[68:71], v113, s[36:39], 0 offen
	v_pk_mul_f32 v[166:167], v[132:133], v[148:149]
	v_pk_fma_f32 v[166:167], v[134:135], v[150:151], v[166:167]
	v_pk_fma_f32 v[166:167], v[136:137], v[152:153], v[166:167]
	v_pk_fma_f32 v[166:167], v[138:139], v[154:155], v[166:167]
	v_pk_fma_f32 v[166:167], v[140:141], v[156:157], v[166:167]
	v_pk_fma_f32 v[166:167], v[142:143], v[158:159], v[166:167]
	v_pk_fma_f32 v[166:167], v[144:145], v[160:161], v[166:167]
	v_pk_fma_f32 v[166:167], v[146:147], v[162:163], v[166:167]
	v_add_f32_e32 v173, v166, v167
	s_waitcnt vmcnt(20)
	v_cvt_pk_f32_fp8_e32 v[116:117], v72
	v_cvt_pk_f32_fp8_sdwa v[118:119], v72 src0_sel:WORD_1
	v_cvt_pk_f32_fp8_e32 v[120:121], v73
	v_cvt_pk_f32_fp8_sdwa v[122:123], v73 src0_sel:WORD_1
	v_cvt_pk_f32_fp8_e32 v[124:125], v74
	v_cvt_pk_f32_fp8_sdwa v[126:127], v74 src0_sel:WORD_1
	v_cvt_pk_f32_fp8_e32 v[128:129], v75
	v_cvt_pk_f32_fp8_sdwa v[130:131], v75 src0_sel:WORD_1
	v_mad_u32_u16 v112, v19, s46, v1
	buffer_load_dwordx4 v[72:75], v112, s[36:39], 0 offen
	v_pk_mul_f32 v[164:165], v[116:117], v[148:149]
	v_pk_fma_f32 v[164:165], v[118:119], v[150:151], v[164:165]
	v_pk_fma_f32 v[164:165], v[120:121], v[152:153], v[164:165]
	v_pk_fma_f32 v[164:165], v[122:123], v[154:155], v[164:165]
	v_pk_fma_f32 v[164:165], v[124:125], v[156:157], v[164:165]
	v_pk_fma_f32 v[164:165], v[126:127], v[158:159], v[164:165]
	v_pk_fma_f32 v[164:165], v[128:129], v[160:161], v[164:165]
	v_pk_fma_f32 v[164:165], v[130:131], v[162:163], v[164:165]
	v_add_f32_e32 v174, v164, v165
	s_waitcnt vmcnt(20)
	v_cvt_pk_f32_fp8_e32 v[132:133], v76
	v_cvt_pk_f32_fp8_sdwa v[134:135], v76 src0_sel:WORD_1
	v_cvt_pk_f32_fp8_e32 v[136:137], v77
	v_cvt_pk_f32_fp8_sdwa v[138:139], v77 src0_sel:WORD_1
	v_cvt_pk_f32_fp8_e32 v[140:141], v78
	v_cvt_pk_f32_fp8_sdwa v[142:143], v78 src0_sel:WORD_1
	v_cvt_pk_f32_fp8_e32 v[144:145], v79
	v_cvt_pk_f32_fp8_sdwa v[146:147], v79 src0_sel:WORD_1
	v_mad_u32_u16 v113, v19, s46, v1 op_sel:[1,0,0,0]
	buffer_load_dwordx4 v[76:79], v113, s[36:39], 0 offen
	v_pk_mul_f32 v[166:167], v[132:133], v[148:149]
	v_pk_fma_f32 v[166:167], v[134:135], v[150:151], v[166:167]
	v_pk_fma_f32 v[166:167], v[136:137], v[152:153], v[166:167]
	v_pk_fma_f32 v[166:167], v[138:139], v[154:155], v[166:167]
	v_pk_fma_f32 v[166:167], v[140:141], v[156:157], v[166:167]
	v_pk_fma_f32 v[166:167], v[142:143], v[158:159], v[166:167]
	v_pk_fma_f32 v[166:167], v[144:145], v[160:161], v[166:167]
	v_pk_fma_f32 v[166:167], v[146:147], v[162:163], v[166:167]
	v_add_f32_e32 v175, v166, v167
	s_waitcnt vmcnt(20)
	v_cvt_pk_f32_fp8_e32 v[116:117], v80
	v_cvt_pk_f32_fp8_sdwa v[118:119], v80 src0_sel:WORD_1
	v_cvt_pk_f32_fp8_e32 v[120:121], v81
	v_cvt_pk_f32_fp8_sdwa v[122:123], v81 src0_sel:WORD_1
	v_cvt_pk_f32_fp8_e32 v[124:125], v82
	v_cvt_pk_f32_fp8_sdwa v[126:127], v82 src0_sel:WORD_1
	v_cvt_pk_f32_fp8_e32 v[128:129], v83
	v_cvt_pk_f32_fp8_sdwa v[130:131], v83 src0_sel:WORD_1
	v_mad_u32_u16 v112, v20, s46, v1
	buffer_load_dwordx4 v[80:83], v112, s[36:39], 0 offen
	v_pk_mul_f32 v[164:165], v[116:117], v[148:149]
	v_pk_fma_f32 v[164:165], v[118:119], v[150:151], v[164:165]
	v_pk_fma_f32 v[164:165], v[120:121], v[152:153], v[164:165]
	v_pk_fma_f32 v[164:165], v[122:123], v[154:155], v[164:165]
	v_pk_fma_f32 v[164:165], v[124:125], v[156:157], v[164:165]
	v_pk_fma_f32 v[164:165], v[126:127], v[158:159], v[164:165]
	v_pk_fma_f32 v[164:165], v[128:129], v[160:161], v[164:165]
	v_pk_fma_f32 v[164:165], v[130:131], v[162:163], v[164:165]
	v_add_f32_e32 v176, v164, v165
	s_waitcnt vmcnt(20)
	v_cvt_pk_f32_fp8_e32 v[132:133], v84
	v_cvt_pk_f32_fp8_sdwa v[134:135], v84 src0_sel:WORD_1
	v_cvt_pk_f32_fp8_e32 v[136:137], v85
	v_cvt_pk_f32_fp8_sdwa v[138:139], v85 src0_sel:WORD_1
	v_cvt_pk_f32_fp8_e32 v[140:141], v86
	v_cvt_pk_f32_fp8_sdwa v[142:143], v86 src0_sel:WORD_1
	v_cvt_pk_f32_fp8_e32 v[144:145], v87
	v_cvt_pk_f32_fp8_sdwa v[146:147], v87 src0_sel:WORD_1
	v_mad_u32_u16 v113, v20, s46, v1 op_sel:[1,0,0,0]
	buffer_load_dwordx4 v[84:87], v113, s[36:39], 0 offen
	v_pk_mul_f32 v[166:167], v[132:133], v[148:149]
	v_pk_fma_f32 v[166:167], v[134:135], v[150:151], v[166:167]
	v_pk_fma_f32 v[166:167], v[136:137], v[152:153], v[166:167]
	v_pk_fma_f32 v[166:167], v[138:139], v[154:155], v[166:167]
	v_pk_fma_f32 v[166:167], v[140:141], v[156:157], v[166:167]
	v_pk_fma_f32 v[166:167], v[142:143], v[158:159], v[166:167]
	v_pk_fma_f32 v[166:167], v[144:145], v[160:161], v[166:167]
	v_pk_fma_f32 v[166:167], v[146:147], v[162:163], v[166:167]
	v_add_f32_e32 v177, v166, v167
	s_waitcnt vmcnt(20)
	v_cvt_pk_f32_fp8_e32 v[116:117], v88
	v_cvt_pk_f32_fp8_sdwa v[118:119], v88 src0_sel:WORD_1
	v_cvt_pk_f32_fp8_e32 v[120:121], v89
	v_cvt_pk_f32_fp8_sdwa v[122:123], v89 src0_sel:WORD_1
	v_cvt_pk_f32_fp8_e32 v[124:125], v90
	v_cvt_pk_f32_fp8_sdwa v[126:127], v90 src0_sel:WORD_1
	v_cvt_pk_f32_fp8_e32 v[128:129], v91
	v_cvt_pk_f32_fp8_sdwa v[130:131], v91 src0_sel:WORD_1
	v_mad_u32_u16 v112, v21, s46, v1
	buffer_load_dwordx4 v[88:91], v112, s[36:39], 0 offen
	v_pk_mul_f32 v[164:165], v[116:117], v[148:149]
	v_pk_fma_f32 v[164:165], v[118:119], v[150:151], v[164:165]
	v_pk_fma_f32 v[164:165], v[120:121], v[152:153], v[164:165]
	v_pk_fma_f32 v[164:165], v[122:123], v[154:155], v[164:165]
	v_pk_fma_f32 v[164:165], v[124:125], v[156:157], v[164:165]
	v_pk_fma_f32 v[164:165], v[126:127], v[158:159], v[164:165]
	v_pk_fma_f32 v[164:165], v[128:129], v[160:161], v[164:165]
	v_pk_fma_f32 v[164:165], v[130:131], v[162:163], v[164:165]
	v_add_f32_e32 v178, v164, v165
	s_waitcnt vmcnt(20)
	v_cvt_pk_f32_fp8_e32 v[132:133], v92
	v_cvt_pk_f32_fp8_sdwa v[134:135], v92 src0_sel:WORD_1
	v_cvt_pk_f32_fp8_e32 v[136:137], v93
	v_cvt_pk_f32_fp8_sdwa v[138:139], v93 src0_sel:WORD_1
	v_cvt_pk_f32_fp8_e32 v[140:141], v94
	v_cvt_pk_f32_fp8_sdwa v[142:143], v94 src0_sel:WORD_1
	v_cvt_pk_f32_fp8_e32 v[144:145], v95
	v_cvt_pk_f32_fp8_sdwa v[146:147], v95 src0_sel:WORD_1
	v_mad_u32_u16 v113, v21, s46, v1 op_sel:[1,0,0,0]
	buffer_load_dwordx4 v[92:95], v113, s[36:39], 0 offen
	v_pk_mul_f32 v[166:167], v[132:133], v[148:149]
	v_pk_fma_f32 v[166:167], v[134:135], v[150:151], v[166:167]
	v_pk_fma_f32 v[166:167], v[136:137], v[152:153], v[166:167]
	v_pk_fma_f32 v[166:167], v[138:139], v[154:155], v[166:167]
	v_pk_fma_f32 v[166:167], v[140:141], v[156:157], v[166:167]
	v_pk_fma_f32 v[166:167], v[142:143], v[158:159], v[166:167]
	v_pk_fma_f32 v[166:167], v[144:145], v[160:161], v[166:167]
	v_pk_fma_f32 v[166:167], v[146:147], v[162:163], v[166:167]
	v_add_f32_e32 v179, v166, v167
	s_waitcnt vmcnt(20)
	v_cvt_pk_f32_fp8_e32 v[116:117], v96
	v_cvt_pk_f32_fp8_sdwa v[118:119], v96 src0_sel:WORD_1
	v_cvt_pk_f32_fp8_e32 v[120:121], v97
	v_cvt_pk_f32_fp8_sdwa v[122:123], v97 src0_sel:WORD_1
	v_cvt_pk_f32_fp8_e32 v[124:125], v98
	v_cvt_pk_f32_fp8_sdwa v[126:127], v98 src0_sel:WORD_1
	v_cvt_pk_f32_fp8_e32 v[128:129], v99
	v_cvt_pk_f32_fp8_sdwa v[130:131], v99 src0_sel:WORD_1
	v_mad_u32_u16 v112, v22, s46, v1
	buffer_load_dwordx4 v[96:99], v112, s[36:39], 0 offen
	v_pk_mul_f32 v[164:165], v[116:117], v[148:149]
	v_pk_fma_f32 v[164:165], v[118:119], v[150:151], v[164:165]
	v_pk_fma_f32 v[164:165], v[120:121], v[152:153], v[164:165]
	v_pk_fma_f32 v[164:165], v[122:123], v[154:155], v[164:165]
	v_pk_fma_f32 v[164:165], v[124:125], v[156:157], v[164:165]
	v_pk_fma_f32 v[164:165], v[126:127], v[158:159], v[164:165]
	v_pk_fma_f32 v[164:165], v[128:129], v[160:161], v[164:165]
	v_pk_fma_f32 v[164:165], v[130:131], v[162:163], v[164:165]
	v_add_f32_e32 v180, v164, v165
	s_waitcnt vmcnt(20)
	v_cvt_pk_f32_fp8_e32 v[132:133], v100
	v_cvt_pk_f32_fp8_sdwa v[134:135], v100 src0_sel:WORD_1
	v_cvt_pk_f32_fp8_e32 v[136:137], v101
	v_cvt_pk_f32_fp8_sdwa v[138:139], v101 src0_sel:WORD_1
	v_cvt_pk_f32_fp8_e32 v[140:141], v102
	v_cvt_pk_f32_fp8_sdwa v[142:143], v102 src0_sel:WORD_1
	v_cvt_pk_f32_fp8_e32 v[144:145], v103
	v_cvt_pk_f32_fp8_sdwa v[146:147], v103 src0_sel:WORD_1
	v_mad_u32_u16 v113, v22, s46, v1 op_sel:[1,0,0,0]
	buffer_load_dwordx4 v[100:103], v113, s[36:39], 0 offen
	v_pk_mul_f32 v[166:167], v[132:133], v[148:149]
	v_pk_fma_f32 v[166:167], v[134:135], v[150:151], v[166:167]
	v_pk_fma_f32 v[166:167], v[136:137], v[152:153], v[166:167]
	v_pk_fma_f32 v[166:167], v[138:139], v[154:155], v[166:167]
	v_pk_fma_f32 v[166:167], v[140:141], v[156:157], v[166:167]
	v_pk_fma_f32 v[166:167], v[142:143], v[158:159], v[166:167]
	v_pk_fma_f32 v[166:167], v[144:145], v[160:161], v[166:167]
	v_pk_fma_f32 v[166:167], v[146:147], v[162:163], v[166:167]
	v_add_f32_e32 v181, v166, v167
	s_waitcnt vmcnt(20)
	v_cvt_pk_f32_fp8_e32 v[116:117], v104
	v_cvt_pk_f32_fp8_sdwa v[118:119], v104 src0_sel:WORD_1
	v_cvt_pk_f32_fp8_e32 v[120:121], v105
	v_cvt_pk_f32_fp8_sdwa v[122:123], v105 src0_sel:WORD_1
	v_cvt_pk_f32_fp8_e32 v[124:125], v106
	v_cvt_pk_f32_fp8_sdwa v[126:127], v106 src0_sel:WORD_1
	v_cvt_pk_f32_fp8_e32 v[128:129], v107
	v_cvt_pk_f32_fp8_sdwa v[130:131], v107 src0_sel:WORD_1
	v_mad_u32_u16 v112, v23, s46, v1
	buffer_load_dwordx4 v[104:107], v112, s[36:39], 0 offen
	v_pk_mul_f32 v[164:165], v[116:117], v[148:149]
	v_pk_fma_f32 v[164:165], v[118:119], v[150:151], v[164:165]
	v_pk_fma_f32 v[164:165], v[120:121], v[152:153], v[164:165]
	v_pk_fma_f32 v[164:165], v[122:123], v[154:155], v[164:165]
	v_pk_fma_f32 v[164:165], v[124:125], v[156:157], v[164:165]
	v_pk_fma_f32 v[164:165], v[126:127], v[158:159], v[164:165]
	v_pk_fma_f32 v[164:165], v[128:129], v[160:161], v[164:165]
	v_pk_fma_f32 v[164:165], v[130:131], v[162:163], v[164:165]
	v_add_f32_e32 v182, v164, v165
	s_waitcnt vmcnt(20)
	v_cvt_pk_f32_fp8_e32 v[132:133], v108
	v_cvt_pk_f32_fp8_sdwa v[134:135], v108 src0_sel:WORD_1
	v_cvt_pk_f32_fp8_e32 v[136:137], v109
	v_cvt_pk_f32_fp8_sdwa v[138:139], v109 src0_sel:WORD_1
	v_cvt_pk_f32_fp8_e32 v[140:141], v110
	v_cvt_pk_f32_fp8_sdwa v[142:143], v110 src0_sel:WORD_1
	v_cvt_pk_f32_fp8_e32 v[144:145], v111
	v_cvt_pk_f32_fp8_sdwa v[146:147], v111 src0_sel:WORD_1
	v_mad_u32_u16 v113, v23, s46, v1 op_sel:[1,0,0,0]
	buffer_load_dwordx4 v[108:111], v113, s[36:39], 0 offen
	v_pk_mul_f32 v[166:167], v[132:133], v[148:149]
	v_pk_fma_f32 v[166:167], v[134:135], v[150:151], v[166:167]
	v_pk_fma_f32 v[166:167], v[136:137], v[152:153], v[166:167]
	v_pk_fma_f32 v[166:167], v[138:139], v[154:155], v[166:167]
	v_pk_fma_f32 v[166:167], v[140:141], v[156:157], v[166:167]
	v_pk_fma_f32 v[166:167], v[142:143], v[158:159], v[166:167]
	v_pk_fma_f32 v[166:167], v[144:145], v[160:161], v[166:167]
	v_pk_fma_f32 v[166:167], v[146:147], v[162:163], v[166:167]
	v_add_f32_e32 v183, v166, v167
	s_nop 1
	v_add_f32_dpp v184, v168, v168 row_half_mirror row_mask:0xf bank_mask:0x5
	v_add_f32_dpp v184, v176, v176 row_half_mirror row_mask:0xf bank_mask:0xa
	v_add_f32_dpp v185, v169, v169 row_half_mirror row_mask:0xf bank_mask:0x5
	v_add_f32_dpp v185, v177, v177 row_half_mirror row_mask:0xf bank_mask:0xa
	v_add_f32_dpp v186, v170, v170 row_half_mirror row_mask:0xf bank_mask:0x5
	v_add_f32_dpp v186, v178, v178 row_half_mirror row_mask:0xf bank_mask:0xa
	v_add_f32_dpp v187, v171, v171 row_half_mirror row_mask:0xf bank_mask:0x5
	v_add_f32_dpp v187, v179, v179 row_half_mirror row_mask:0xf bank_mask:0xa
	v_add_f32_dpp v188, v172, v172 row_half_mirror row_mask:0xf bank_mask:0x5
	v_add_f32_dpp v188, v180, v180 row_half_mirror row_mask:0xf bank_mask:0xa
	v_add_f32_dpp v189, v173, v173 row_half_mirror row_mask:0xf bank_mask:0x5
	v_add_f32_dpp v189, v181, v181 row_half_mirror row_mask:0xf bank_mask:0xa
	v_add_f32_dpp v190, v174, v174 row_half_mirror row_mask:0xf bank_mask:0x5
	v_add_f32_dpp v190, v182, v182 row_half_mirror row_mask:0xf bank_mask:0xa
	v_add_f32_dpp v191, v175, v175 row_half_mirror row_mask:0xf bank_mask:0x5
	v_add_f32_dpp v191, v183, v183 row_half_mirror row_mask:0xf bank_mask:0xa
	v_cndmask_b32_e64 v192, v188, v184, s[44:45]
	v_cndmask_b32_e64 v193, v184, v188, s[44:45]
	v_cndmask_b32_e64 v194, v189, v185, s[44:45]
	v_cndmask_b32_e64 v195, v185, v189, s[44:45]
	v_cndmask_b32_e64 v196, v190, v186, s[44:45]
	v_cndmask_b32_e64 v197, v186, v190, s[44:45]
	v_cndmask_b32_e64 v198, v191, v187, s[44:45]
	v_cndmask_b32_e64 v199, v187, v191, s[44:45]
	v_add_f32_dpp v200, v192, v193 quad_perm:[3,2,1,0] row_mask:0xf bank_mask:0xf
	v_add_f32_dpp v201, v194, v195 quad_perm:[3,2,1,0] row_mask:0xf bank_mask:0xf
	v_add_f32_dpp v202, v196, v197 quad_perm:[3,2,1,0] row_mask:0xf bank_mask:0xf
	v_add_f32_dpp v203, v198, v199 quad_perm:[3,2,1,0] row_mask:0xf bank_mask:0xf
	v_cndmask_b32_e64 v204, v202, v200, s[42:43]
	v_cndmask_b32_e64 v205, v200, v202, s[42:43]
	v_cndmask_b32_e64 v206, v203, v201, s[42:43]
	v_cndmask_b32_e64 v207, v201, v203, s[42:43]
	s_nop 0
	v_add_f32_dpp v208, v204, v205 quad_perm:[1,0,3,2] row_mask:0xf bank_mask:0xf
	v_add_f32_dpp v209, v206, v207 quad_perm:[1,0,3,2] row_mask:0xf bank_mask:0xf
	v_cvt_pk_bf16_f32 v210, v208, v209
	s_lshl_b32 s2, s20, 8
	s_add_u32 s2, s34, s2
	s_addc_u32 s3, s35, 0
	global_store_dword v3, v210, s[2:3]
	s_mov_b32 s20, s21
	s_mov_b32 s48, s49
	s_mov_b32 s21, s22
	s_mov_b32 s49, s50
	s_cmp_eq_u32 s48, 0
	s_cbranch_scc1 .Lub_drain
	s_cmp_lg_u32 s26, 32
	s_cbranch_scc1 .Lub_norot_l1
	v_readfirstlane_b32 s23, v6
	s_mov_b64 exec, 1
	global_atomic_inc v6, v5, v7, s[6:7] sc0
	s_mov_b64 exec, -1
	s_mov_b32 s26, 0

.Lub_got_l1:
	s_lshl_b32 s2, s22, 8
	s_add_u32 s2, s28, s2
	s_addc_u32 s3, s29, 0
	global_load_dwordx4 v[16:19], v2, s[2:3]
	global_load_dwordx4 v[20:23], v2, s[2:3] offset:16
	s_lshl_b32 s2, s21, 12
	s_add_u32 s2, s30, s2
	s_addc_u32 s3, s31, 0
	global_load_dwordx4 v[24:27], v4, s[2:3]
	global_load_dwordx4 v[28:31], v4, s[2:3] offset:16
	s_waitcnt vmcnt(20)
	v_cvt_pk_f32_fp8_e32 v[116:117], v48
	v_cvt_pk_f32_fp8_sdwa v[118:119], v48 src0_sel:WORD_1
	v_cvt_pk_f32_fp8_e32 v[120:121], v49
	v_cvt_pk_f32_fp8_sdwa v[122:123], v49 src0_sel:WORD_1
	v_cvt_pk_f32_fp8_e32 v[124:125], v50
	v_cvt_pk_f32_fp8_sdwa v[126:127], v50 src0_sel:WORD_1
	v_cvt_pk_f32_fp8_e32 v[128:129], v51
	v_cvt_pk_f32_fp8_sdwa v[130:131], v51 src0_sel:WORD_1
	v_lshlrev_b32_e32 v148, 16, v32
	v_and_b32_e32 v149, 0xffff0000, v32
	v_lshlrev_b32_e32 v150, 16, v33
	v_and_b32_e32 v151, 0xffff0000, v33
	v_lshlrev_b32_e32 v152, 16, v34
	v_and_b32_e32 v153, 0xffff0000, v34
	v_lshlrev_b32_e32 v154, 16, v35
	v_and_b32_e32 v155, 0xffff0000, v35
	v_lshlrev_b32_e32 v156, 16, v36
	v_and_b32_e32 v157, 0xffff0000, v36
	v_lshlrev_b32_e32 v158, 16, v37
	v_and_b32_e32 v159, 0xffff0000, v37
	v_lshlrev_b32_e32 v160, 16, v38
	v_and_b32_e32 v161, 0xffff0000, v38
	v_lshlrev_b32_e32 v162, 16, v39
	v_and_b32_e32 v163, 0xffff0000, v39
	v_mad_u32_u16 v112, v8, s46, v1
	buffer_load_dwordx4 v[48:51], v112, s[36:39], 0 offen
	v_pk_mul_f32 v[164:165], v[116:117], v[148:149]
	v_pk_fma_f32 v[164:165], v[118:119], v[150:151], v[164:165]
	v_pk_fma_f32 v[164:165], v[120:121], v[152:153], v[164:165]
	v_pk_fma_f32 v[164:165], v[122:123], v[154:155], v[164:165]
	v_pk_fma_f32 v[164:165], v[124:125], v[156:157], v[164:165]
	v_pk_fma_f32 v[164:165], v[126:127], v[158:159], v[164:165]
	v_pk_fma_f32 v[164:165], v[128:129], v[160:161], v[164:165]
	v_pk_fma_f32 v[164:165], v[130:131], v[162:163], v[164:165]
	v_add_f32_e32 v168, v164, v165
	s_waitcnt vmcnt(20)
	v_cvt_pk_f32_fp8_e32 v[132:133], v52
	v_cvt_pk_f32_fp8_sdwa v[134:135], v52 src0_sel:WORD_1
	v_cvt_pk_f32_fp8_e32 v[136:137], v53
	v_cvt_pk_f32_fp8_sdwa v[138:139], v53 src0_sel:WORD_1
	v_cvt_pk_f32_fp8_e32 v[140:141], v54
	v_cvt_pk_f32_fp8_sdwa v[142:143], v54 src0_sel:WORD_1
	v_cvt_pk_f32_fp8_e32 v[144:145], v55
	v_cvt_pk_f32_fp8_sdwa v[146:147], v55 src0_sel:WORD_1
	v_mad_u32_u16 v113, v8, s46, v1 op_sel:[1,0,0,0]
	buffer_load_dwordx4 v[52:55], v113, s[36:39], 0 offen
	v_pk_mul_f32 v[166:167], v[132:133], v[148:149]
	v_pk_fma_f32 v[166:167], v[134:135], v[150:151], v[166:167]
	v_pk_fma_f32 v[166:167], v[136:137], v[152:153], v[166:167]
	v_pk_fma_f32 v[166:167], v[138:139], v[154:155], v[166:167]
	v_pk_fma_f32 v[166:167], v[140:141], v[156:157], v[166:167]
	v_pk_fma_f32 v[166:167], v[142:143], v[158:159], v[166:167]
	v_pk_fma_f32 v[166:167], v[144:145], v[160:161], v[166:167]
	v_pk_fma_f32 v[166:167], v[146:147], v[162:163], v[166:167]
	v_add_f32_e32 v169, v166, v167
	s_waitcnt vmcnt(20)
	v_cvt_pk_f32_fp8_e32 v[116:117], v56
	v_cvt_pk_f32_fp8_sdwa v[118:119], v56 src0_sel:WORD_1
	v_cvt_pk_f32_fp8_e32 v[120:121], v57
	v_cvt_pk_f32_fp8_sdwa v[122:123], v57 src0_sel:WORD_1
	v_cvt_pk_f32_fp8_e32 v[124:125], v58
	v_cvt_pk_f32_fp8_sdwa v[126:127], v58 src0_sel:WORD_1
	v_cvt_pk_f32_fp8_e32 v[128:129], v59
	v_cvt_pk_f32_fp8_sdwa v[130:131], v59 src0_sel:WORD_1
	v_mad_u32_u16 v112, v9, s46, v1
	buffer_load_dwordx4 v[56:59], v112, s[36:39], 0 offen
	v_pk_mul_f32 v[164:165], v[116:117], v[148:149]
	v_pk_fma_f32 v[164:165], v[118:119], v[150:151], v[164:165]
	v_pk_fma_f32 v[164:165], v[120:121], v[152:153], v[164:165]
	v_pk_fma_f32 v[164:165], v[122:123], v[154:155], v[164:165]
	v_pk_fma_f32 v[164:165], v[124:125], v[156:157], v[164:165]
	v_pk_fma_f32 v[164:165], v[126:127], v[158:159], v[164:165]
	v_pk_fma_f32 v[164:165], v[128:129], v[160:161], v[164:165]
	v_pk_fma_f32 v[164:165], v[130:131], v[162:163], v[164:165]
	v_add_f32_e32 v170, v164, v165
	s_waitcnt vmcnt(20)
	v_cvt_pk_f32_fp8_e32 v[132:133], v60
	v_cvt_pk_f32_fp8_sdwa v[134:135], v60 src0_sel:WORD_1
	v_cvt_pk_f32_fp8_e32 v[136:137], v61
	v_cvt_pk_f32_fp8_sdwa v[138:139], v61 src0_sel:WORD_1
	v_cvt_pk_f32_fp8_e32 v[140:141], v62
	v_cvt_pk_f32_fp8_sdwa v[142:143], v62 src0_sel:WORD_1
	v_cvt_pk_f32_fp8_e32 v[144:145], v63
	v_cvt_pk_f32_fp8_sdwa v[146:147], v63 src0_sel:WORD_1
	v_mad_u32_u16 v113, v9, s46, v1 op_sel:[1,0,0,0]
	buffer_load_dwordx4 v[60:63], v113, s[36:39], 0 offen
	v_pk_mul_f32 v[166:167], v[132:133], v[148:149]
	v_pk_fma_f32 v[166:167], v[134:135], v[150:151], v[166:167]
	v_pk_fma_f32 v[166:167], v[136:137], v[152:153], v[166:167]
	v_pk_fma_f32 v[166:167], v[138:139], v[154:155], v[166:167]
	v_pk_fma_f32 v[166:167], v[140:141], v[156:157], v[166:167]
	v_pk_fma_f32 v[166:167], v[142:143], v[158:159], v[166:167]
	v_pk_fma_f32 v[166:167], v[144:145], v[160:161], v[166:167]
	v_pk_fma_f32 v[166:167], v[146:147], v[162:163], v[166:167]
	v_add_f32_e32 v171, v166, v167
	s_waitcnt vmcnt(20)
	v_cvt_pk_f32_fp8_e32 v[116:117], v64
	v_cvt_pk_f32_fp8_sdwa v[118:119], v64 src0_sel:WORD_1
	v_cvt_pk_f32_fp8_e32 v[120:121], v65
	v_cvt_pk_f32_fp8_sdwa v[122:123], v65 src0_sel:WORD_1
	v_cvt_pk_f32_fp8_e32 v[124:125], v66
	v_cvt_pk_f32_fp8_sdwa v[126:127], v66 src0_sel:WORD_1
	v_cvt_pk_f32_fp8_e32 v[128:129], v67
	v_cvt_pk_f32_fp8_sdwa v[130:131], v67 src0_sel:WORD_1
	v_mad_u32_u16 v112, v10, s46, v1
	buffer_load_dwordx4 v[64:67], v112, s[36:39], 0 offen
	v_pk_mul_f32 v[164:165], v[116:117], v[148:149]
	v_pk_fma_f32 v[164:165], v[118:119], v[150:151], v[164:165]
	v_pk_fma_f32 v[164:165], v[120:121], v[152:153], v[164:165]
	v_pk_fma_f32 v[164:165], v[122:123], v[154:155], v[164:165]
	v_pk_fma_f32 v[164:165], v[124:125], v[156:157], v[164:165]
	v_pk_fma_f32 v[164:165], v[126:127], v[158:159], v[164:165]
	v_pk_fma_f32 v[164:165], v[128:129], v[160:161], v[164:165]
	v_pk_fma_f32 v[164:165], v[130:131], v[162:163], v[164:165]
	v_add_f32_e32 v172, v164, v165
	s_waitcnt vmcnt(20)
	v_cvt_pk_f32_fp8_e32 v[132:133], v68
	v_cvt_pk_f32_fp8_sdwa v[134:135], v68 src0_sel:WORD_1
	v_cvt_pk_f32_fp8_e32 v[136:137], v69
	v_cvt_pk_f32_fp8_sdwa v[138:139], v69 src0_sel:WORD_1
	v_cvt_pk_f32_fp8_e32 v[140:141], v70
	v_cvt_pk_f32_fp8_sdwa v[142:143], v70 src0_sel:WORD_1
	v_cvt_pk_f32_fp8_e32 v[144:145], v71
	v_cvt_pk_f32_fp8_sdwa v[146:147], v71 src0_sel:WORD_1
	v_mad_u32_u16 v113, v10, s46, v1 op_sel:[1,0,0,0]
	buffer_load_dwordx4 v[68:71], v113, s[36:39], 0 offen
	v_pk_mul_f32 v[166:167], v[132:133], v[148:149]
	v_pk_fma_f32 v[166:167], v[134:135], v[150:151], v[166:167]
	v_pk_fma_f32 v[166:167], v[136:137], v[152:153], v[166:167]
	v_pk_fma_f32 v[166:167], v[138:139], v[154:155], v[166:167]
	v_pk_fma_f32 v[166:167], v[140:141], v[156:157], v[166:167]
	v_pk_fma_f32 v[166:167], v[142:143], v[158:159], v[166:167]
	v_pk_fma_f32 v[166:167], v[144:145], v[160:161], v[166:167]
	v_pk_fma_f32 v[166:167], v[146:147], v[162:163], v[166:167]
	v_add_f32_e32 v173, v166, v167
	s_waitcnt vmcnt(20)
	v_cvt_pk_f32_fp8_e32 v[116:117], v72
	v_cvt_pk_f32_fp8_sdwa v[118:119], v72 src0_sel:WORD_1
	v_cvt_pk_f32_fp8_e32 v[120:121], v73
	v_cvt_pk_f32_fp8_sdwa v[122:123], v73 src0_sel:WORD_1
	v_cvt_pk_f32_fp8_e32 v[124:125], v74
	v_cvt_pk_f32_fp8_sdwa v[126:127], v74 src0_sel:WORD_1
	v_cvt_pk_f32_fp8_e32 v[128:129], v75
	v_cvt_pk_f32_fp8_sdwa v[130:131], v75 src0_sel:WORD_1
	v_mad_u32_u16 v112, v11, s46, v1
	buffer_load_dwordx4 v[72:75], v112, s[36:39], 0 offen
	v_pk_mul_f32 v[164:165], v[116:117], v[148:149]
	v_pk_fma_f32 v[164:165], v[118:119], v[150:151], v[164:165]
	v_pk_fma_f32 v[164:165], v[120:121], v[152:153], v[164:165]
	v_pk_fma_f32 v[164:165], v[122:123], v[154:155], v[164:165]
	v_pk_fma_f32 v[164:165], v[124:125], v[156:157], v[164:165]
	v_pk_fma_f32 v[164:165], v[126:127], v[158:159], v[164:165]
	v_pk_fma_f32 v[164:165], v[128:129], v[160:161], v[164:165]
	v_pk_fma_f32 v[164:165], v[130:131], v[162:163], v[164:165]
	v_add_f32_e32 v174, v164, v165
	s_waitcnt vmcnt(20)
	v_cvt_pk_f32_fp8_e32 v[132:133], v76
	v_cvt_pk_f32_fp8_sdwa v[134:135], v76 src0_sel:WORD_1
	v_cvt_pk_f32_fp8_e32 v[136:137], v77
	v_cvt_pk_f32_fp8_sdwa v[138:139], v77 src0_sel:WORD_1
	v_cvt_pk_f32_fp8_e32 v[140:141], v78
	v_cvt_pk_f32_fp8_sdwa v[142:143], v78 src0_sel:WORD_1
	v_cvt_pk_f32_fp8_e32 v[144:145], v79
	v_cvt_pk_f32_fp8_sdwa v[146:147], v79 src0_sel:WORD_1
	v_mad_u32_u16 v113, v11, s46, v1 op_sel:[1,0,0,0]
	buffer_load_dwordx4 v[76:79], v113, s[36:39], 0 offen
	v_pk_mul_f32 v[166:167], v[132:133], v[148:149]
	v_pk_fma_f32 v[166:167], v[134:135], v[150:151], v[166:167]
	v_pk_fma_f32 v[166:167], v[136:137], v[152:153], v[166:167]
	v_pk_fma_f32 v[166:167], v[138:139], v[154:155], v[166:167]
	v_pk_fma_f32 v[166:167], v[140:141], v[156:157], v[166:167]
	v_pk_fma_f32 v[166:167], v[142:143], v[158:159], v[166:167]
	v_pk_fma_f32 v[166:167], v[144:145], v[160:161], v[166:167]
	v_pk_fma_f32 v[166:167], v[146:147], v[162:163], v[166:167]
	v_add_f32_e32 v175, v166, v167
	s_waitcnt vmcnt(20)
	v_cvt_pk_f32_fp8_e32 v[116:117], v80
	v_cvt_pk_f32_fp8_sdwa v[118:119], v80 src0_sel:WORD_1
	v_cvt_pk_f32_fp8_e32 v[120:121], v81
	v_cvt_pk_f32_fp8_sdwa v[122:123], v81 src0_sel:WORD_1
	v_cvt_pk_f32_fp8_e32 v[124:125], v82
	v_cvt_pk_f32_fp8_sdwa v[126:127], v82 src0_sel:WORD_1
	v_cvt_pk_f32_fp8_e32 v[128:129], v83
	v_cvt_pk_f32_fp8_sdwa v[130:131], v83 src0_sel:WORD_1
	v_mad_u32_u16 v112, v12, s46, v1
	buffer_load_dwordx4 v[80:83], v112, s[36:39], 0 offen
	v_pk_mul_f32 v[164:165], v[116:117], v[148:149]
	v_pk_fma_f32 v[164:165], v[118:119], v[150:151], v[164:165]
	v_pk_fma_f32 v[164:165], v[120:121], v[152:153], v[164:165]
	v_pk_fma_f32 v[164:165], v[122:123], v[154:155], v[164:165]
	v_pk_fma_f32 v[164:165], v[124:125], v[156:157], v[164:165]
	v_pk_fma_f32 v[164:165], v[126:127], v[158:159], v[164:165]
	v_pk_fma_f32 v[164:165], v[128:129], v[160:161], v[164:165]
	v_pk_fma_f32 v[164:165], v[130:131], v[162:163], v[164:165]
	v_add_f32_e32 v176, v164, v165
	s_waitcnt vmcnt(20)
	v_cvt_pk_f32_fp8_e32 v[132:133], v84
	v_cvt_pk_f32_fp8_sdwa v[134:135], v84 src0_sel:WORD_1
	v_cvt_pk_f32_fp8_e32 v[136:137], v85
	v_cvt_pk_f32_fp8_sdwa v[138:139], v85 src0_sel:WORD_1
	v_cvt_pk_f32_fp8_e32 v[140:141], v86
	v_cvt_pk_f32_fp8_sdwa v[142:143], v86 src0_sel:WORD_1
	v_cvt_pk_f32_fp8_e32 v[144:145], v87
	v_cvt_pk_f32_fp8_sdwa v[146:147], v87 src0_sel:WORD_1
	v_mad_u32_u16 v113, v12, s46, v1 op_sel:[1,0,0,0]
	buffer_load_dwordx4 v[84:87], v113, s[36:39], 0 offen
	v_pk_mul_f32 v[166:167], v[132:133], v[148:149]
	v_pk_fma_f32 v[166:167], v[134:135], v[150:151], v[166:167]
	v_pk_fma_f32 v[166:167], v[136:137], v[152:153], v[166:167]
	v_pk_fma_f32 v[166:167], v[138:139], v[154:155], v[166:167]
	v_pk_fma_f32 v[166:167], v[140:141], v[156:157], v[166:167]
	v_pk_fma_f32 v[166:167], v[142:143], v[158:159], v[166:167]
	v_pk_fma_f32 v[166:167], v[144:145], v[160:161], v[166:167]
	v_pk_fma_f32 v[166:167], v[146:147], v[162:163], v[166:167]
	v_add_f32_e32 v177, v166, v167
	s_waitcnt vmcnt(20)
	v_cvt_pk_f32_fp8_e32 v[116:117], v88
	v_cvt_pk_f32_fp8_sdwa v[118:119], v88 src0_sel:WORD_1
	v_cvt_pk_f32_fp8_e32 v[120:121], v89
	v_cvt_pk_f32_fp8_sdwa v[122:123], v89 src0_sel:WORD_1
	v_cvt_pk_f32_fp8_e32 v[124:125], v90
	v_cvt_pk_f32_fp8_sdwa v[126:127], v90 src0_sel:WORD_1
	v_cvt_pk_f32_fp8_e32 v[128:129], v91
	v_cvt_pk_f32_fp8_sdwa v[130:131], v91 src0_sel:WORD_1
	v_mad_u32_u16 v112, v13, s46, v1
	buffer_load_dwordx4 v[88:91], v112, s[36:39], 0 offen
	v_pk_mul_f32 v[164:165], v[116:117], v[148:149]
	v_pk_fma_f32 v[164:165], v[118:119], v[150:151], v[164:165]
	v_pk_fma_f32 v[164:165], v[120:121], v[152:153], v[164:165]
	v_pk_fma_f32 v[164:165], v[122:123], v[154:155], v[164:165]
	v_pk_fma_f32 v[164:165], v[124:125], v[156:157], v[164:165]
	v_pk_fma_f32 v[164:165], v[126:127], v[158:159], v[164:165]
	v_pk_fma_f32 v[164:165], v[128:129], v[160:161], v[164:165]
	v_pk_fma_f32 v[164:165], v[130:131], v[162:163], v[164:165]
	v_add_f32_e32 v178, v164, v165
	s_waitcnt vmcnt(20)
	v_cvt_pk_f32_fp8_e32 v[132:133], v92
	v_cvt_pk_f32_fp8_sdwa v[134:135], v92 src0_sel:WORD_1
	v_cvt_pk_f32_fp8_e32 v[136:137], v93
	v_cvt_pk_f32_fp8_sdwa v[138:139], v93 src0_sel:WORD_1
	v_cvt_pk_f32_fp8_e32 v[140:141], v94
	v_cvt_pk_f32_fp8_sdwa v[142:143], v94 src0_sel:WORD_1
	v_cvt_pk_f32_fp8_e32 v[144:145], v95
	v_cvt_pk_f32_fp8_sdwa v[146:147], v95 src0_sel:WORD_1
	v_mad_u32_u16 v113, v13, s46, v1 op_sel:[1,0,0,0]
	buffer_load_dwordx4 v[92:95], v113, s[36:39], 0 offen
	v_pk_mul_f32 v[166:167], v[132:133], v[148:149]
	v_pk_fma_f32 v[166:167], v[134:135], v[150:151], v[166:167]
	v_pk_fma_f32 v[166:167], v[136:137], v[152:153], v[166:167]
	v_pk_fma_f32 v[166:167], v[138:139], v[154:155], v[166:167]
	v_pk_fma_f32 v[166:167], v[140:141], v[156:157], v[166:167]
	v_pk_fma_f32 v[166:167], v[142:143], v[158:159], v[166:167]
	v_pk_fma_f32 v[166:167], v[144:145], v[160:161], v[166:167]
	v_pk_fma_f32 v[166:167], v[146:147], v[162:163], v[166:167]
	v_add_f32_e32 v179, v166, v167
	s_waitcnt vmcnt(20)
	v_cvt_pk_f32_fp8_e32 v[116:117], v96
	v_cvt_pk_f32_fp8_sdwa v[118:119], v96 src0_sel:WORD_1
	v_cvt_pk_f32_fp8_e32 v[120:121], v97
	v_cvt_pk_f32_fp8_sdwa v[122:123], v97 src0_sel:WORD_1
	v_cvt_pk_f32_fp8_e32 v[124:125], v98
	v_cvt_pk_f32_fp8_sdwa v[126:127], v98 src0_sel:WORD_1
	v_cvt_pk_f32_fp8_e32 v[128:129], v99
	v_cvt_pk_f32_fp8_sdwa v[130:131], v99 src0_sel:WORD_1
	v_mad_u32_u16 v112, v14, s46, v1
	buffer_load_dwordx4 v[96:99], v112, s[36:39], 0 offen
	v_pk_mul_f32 v[164:165], v[116:117], v[148:149]
	v_pk_fma_f32 v[164:165], v[118:119], v[150:151], v[164:165]
	v_pk_fma_f32 v[164:165], v[120:121], v[152:153], v[164:165]
	v_pk_fma_f32 v[164:165], v[122:123], v[154:155], v[164:165]
	v_pk_fma_f32 v[164:165], v[124:125], v[156:157], v[164:165]
	v_pk_fma_f32 v[164:165], v[126:127], v[158:159], v[164:165]
	v_pk_fma_f32 v[164:165], v[128:129], v[160:161], v[164:165]
	v_pk_fma_f32 v[164:165], v[130:131], v[162:163], v[164:165]
	v_add_f32_e32 v180, v164, v165
	s_waitcnt vmcnt(20)
	v_cvt_pk_f32_fp8_e32 v[132:133], v100
	v_cvt_pk_f32_fp8_sdwa v[134:135], v100 src0_sel:WORD_1
	v_cvt_pk_f32_fp8_e32 v[136:137], v101
	v_cvt_pk_f32_fp8_sdwa v[138:139], v101 src0_sel:WORD_1
	v_cvt_pk_f32_fp8_e32 v[140:141], v102
	v_cvt_pk_f32_fp8_sdwa v[142:143], v102 src0_sel:WORD_1
	v_cvt_pk_f32_fp8_e32 v[144:145], v103
	v_cvt_pk_f32_fp8_sdwa v[146:147], v103 src0_sel:WORD_1
	v_mad_u32_u16 v113, v14, s46, v1 op_sel:[1,0,0,0]
	buffer_load_dwordx4 v[100:103], v113, s[36:39], 0 offen
	v_pk_mul_f32 v[166:167], v[132:133], v[148:149]
	v_pk_fma_f32 v[166:167], v[134:135], v[150:151], v[166:167]
	v_pk_fma_f32 v[166:167], v[136:137], v[152:153], v[166:167]
	v_pk_fma_f32 v[166:167], v[138:139], v[154:155], v[166:167]
	v_pk_fma_f32 v[166:167], v[140:141], v[156:157], v[166:167]
	v_pk_fma_f32 v[166:167], v[142:143], v[158:159], v[166:167]
	v_pk_fma_f32 v[166:167], v[144:145], v[160:161], v[166:167]
	v_pk_fma_f32 v[166:167], v[146:147], v[162:163], v[166:167]
	v_add_f32_e32 v181, v166, v167
	s_waitcnt vmcnt(20)
	v_cvt_pk_f32_fp8_e32 v[116:117], v104
	v_cvt_pk_f32_fp8_sdwa v[118:119], v104 src0_sel:WORD_1
	v_cvt_pk_f32_fp8_e32 v[120:121], v105
	v_cvt_pk_f32_fp8_sdwa v[122:123], v105 src0_sel:WORD_1
	v_cvt_pk_f32_fp8_e32 v[124:125], v106
	v_cvt_pk_f32_fp8_sdwa v[126:127], v106 src0_sel:WORD_1
	v_cvt_pk_f32_fp8_e32 v[128:129], v107
	v_cvt_pk_f32_fp8_sdwa v[130:131], v107 src0_sel:WORD_1
	v_mad_u32_u16 v112, v15, s46, v1
	buffer_load_dwordx4 v[104:107], v112, s[36:39], 0 offen
	v_pk_mul_f32 v[164:165], v[116:117], v[148:149]
	v_pk_fma_f32 v[164:165], v[118:119], v[150:151], v[164:165]
	v_pk_fma_f32 v[164:165], v[120:121], v[152:153], v[164:165]
	v_pk_fma_f32 v[164:165], v[122:123], v[154:155], v[164:165]
	v_pk_fma_f32 v[164:165], v[124:125], v[156:157], v[164:165]
	v_pk_fma_f32 v[164:165], v[126:127], v[158:159], v[164:165]
	v_pk_fma_f32 v[164:165], v[128:129], v[160:161], v[164:165]
	v_pk_fma_f32 v[164:165], v[130:131], v[162:163], v[164:165]
	v_add_f32_e32 v182, v164, v165
	s_waitcnt vmcnt(20)
	v_cvt_pk_f32_fp8_e32 v[132:133], v108
	v_cvt_pk_f32_fp8_sdwa v[134:135], v108 src0_sel:WORD_1
	v_cvt_pk_f32_fp8_e32 v[136:137], v109
	v_cvt_pk_f32_fp8_sdwa v[138:139], v109 src0_sel:WORD_1
	v_cvt_pk_f32_fp8_e32 v[140:141], v110
	v_cvt_pk_f32_fp8_sdwa v[142:143], v110 src0_sel:WORD_1
	v_cvt_pk_f32_fp8_e32 v[144:145], v111
	v_cvt_pk_f32_fp8_sdwa v[146:147], v111 src0_sel:WORD_1
	v_mad_u32_u16 v113, v15, s46, v1 op_sel:[1,0,0,0]
	buffer_load_dwordx4 v[108:111], v113, s[36:39], 0 offen
	v_pk_mul_f32 v[166:167], v[132:133], v[148:149]
	v_pk_fma_f32 v[166:167], v[134:135], v[150:151], v[166:167]
	v_pk_fma_f32 v[166:167], v[136:137], v[152:153], v[166:167]
	v_pk_fma_f32 v[166:167], v[138:139], v[154:155], v[166:167]
	v_pk_fma_f32 v[166:167], v[140:141], v[156:157], v[166:167]
	v_pk_fma_f32 v[166:167], v[142:143], v[158:159], v[166:167]
	v_pk_fma_f32 v[166:167], v[144:145], v[160:161], v[166:167]
	v_pk_fma_f32 v[166:167], v[146:147], v[162:163], v[166:167]
	v_add_f32_e32 v183, v166, v167
	s_nop 1
	v_add_f32_dpp v184, v168, v168 row_half_mirror row_mask:0xf bank_mask:0x5
	v_add_f32_dpp v184, v176, v176 row_half_mirror row_mask:0xf bank_mask:0xa
	v_add_f32_dpp v185, v169, v169 row_half_mirror row_mask:0xf bank_mask:0x5
	v_add_f32_dpp v185, v177, v177 row_half_mirror row_mask:0xf bank_mask:0xa
	v_add_f32_dpp v186, v170, v170 row_half_mirror row_mask:0xf bank_mask:0x5
	v_add_f32_dpp v186, v178, v178 row_half_mirror row_mask:0xf bank_mask:0xa
	v_add_f32_dpp v187, v171, v171 row_half_mirror row_mask:0xf bank_mask:0x5
	v_add_f32_dpp v187, v179, v179 row_half_mirror row_mask:0xf bank_mask:0xa
	v_add_f32_dpp v188, v172, v172 row_half_mirror row_mask:0xf bank_mask:0x5
	v_add_f32_dpp v188, v180, v180 row_half_mirror row_mask:0xf bank_mask:0xa
	v_add_f32_dpp v189, v173, v173 row_half_mirror row_mask:0xf bank_mask:0x5
	v_add_f32_dpp v189, v181, v181 row_half_mirror row_mask:0xf bank_mask:0xa
	v_add_f32_dpp v190, v174, v174 row_half_mirror row_mask:0xf bank_mask:0x5
	v_add_f32_dpp v190, v182, v182 row_half_mirror row_mask:0xf bank_mask:0xa
	v_add_f32_dpp v191, v175, v175 row_half_mirror row_mask:0xf bank_mask:0x5
	v_add_f32_dpp v191, v183, v183 row_half_mirror row_mask:0xf bank_mask:0xa
	v_cndmask_b32_e64 v192, v188, v184, s[44:45]
	v_cndmask_b32_e64 v193, v184, v188, s[44:45]
	v_cndmask_b32_e64 v194, v189, v185, s[44:45]
	v_cndmask_b32_e64 v195, v185, v189, s[44:45]
	v_cndmask_b32_e64 v196, v190, v186, s[44:45]
	v_cndmask_b32_e64 v197, v186, v190, s[44:45]
	v_cndmask_b32_e64 v198, v191, v187, s[44:45]
	v_cndmask_b32_e64 v199, v187, v191, s[44:45]
	v_add_f32_dpp v200, v192, v193 quad_perm:[3,2,1,0] row_mask:0xf bank_mask:0xf
	v_add_f32_dpp v201, v194, v195 quad_perm:[3,2,1,0] row_mask:0xf bank_mask:0xf
	v_add_f32_dpp v202, v196, v197 quad_perm:[3,2,1,0] row_mask:0xf bank_mask:0xf
	v_add_f32_dpp v203, v198, v199 quad_perm:[3,2,1,0] row_mask:0xf bank_mask:0xf
	v_cndmask_b32_e64 v204, v202, v200, s[42:43]
	v_cndmask_b32_e64 v205, v200, v202, s[42:43]
	v_cndmask_b32_e64 v206, v203, v201, s[42:43]
	v_cndmask_b32_e64 v207, v201, v203, s[42:43]
	s_nop 0
	v_add_f32_dpp v208, v204, v205 quad_perm:[1,0,3,2] row_mask:0xf bank_mask:0xf
	v_add_f32_dpp v209, v206, v207 quad_perm:[1,0,3,2] row_mask:0xf bank_mask:0xf
	v_cvt_pk_bf16_f32 v210, v208, v209
	s_lshl_b32 s2, s20, 8
	s_add_u32 s2, s34, s2
	s_addc_u32 s3, s35, 0
	global_store_dword v3, v210, s[2:3]
	s_mov_b32 s20, s21
	s_mov_b32 s48, s49
	s_mov_b32 s21, s22
	s_mov_b32 s49, s50
	s_cmp_eq_u32 s48, 0
	s_cbranch_scc1 .Lub_drain
	s_branch .Lub_loop

.LBB0_1188:
	s_cmp_lt_i32 s40, 13
	s_cselect_b64 s[2:3], -1, 0
	s_and_b64 s[14:15], s[2:3], s[4:5]
	s_andn2_b64 vcc, exec, s[14:15]
	s_cbranch_vccnz .LBB0_1215
	s_mov_b64 s[2:3], s[0:1]
	s_waitcnt vmcnt(0) lgkmcnt(0)
	v_mbcnt_lo_u32_b32 v0, -1, 0
	v_mbcnt_hi_u32_b32 v0, -1, v0
	s_load_dwordx2 s[4:5], s[2:3], 0xb8
	s_load_dwordx4 s[56:59], s[2:3], 0xa8
	s_load_dwordx2 s[60:61], s[2:3], 0x20
	s_mov_b32 s51, 0
	s_mov_b32 s52, 0
	s_mov_b32 s53, 0
	s_mov_b32 s75, 0
	v_and_b32_e32 v9, 7, v0
	v_lshrrev_b32_e32 v10, 3, v0
	v_lshlrev_b32_e32 v1, 4, v9
	v_lshlrev_b32_e32 v2, 5, v10
	v_lshlrev_b32_e32 v3, 5, v9
	v_and_b32_e32 v11, 56, v0
	v_lshrrev_b32_e32 v11, 1, v11
	v_or_b32_e32 v3, v3, v11
	v_and_b32_e32 v12, 8, v0
	v_cmp_eq_u32_e64 s[44:45], 0, v12
	v_and_b32_e32 v12, 24, v0
	v_cmp_eq_u32_e64 s[42:43], 0, v12
	v_mov_b32_e32 v5, 0
	v_mov_b32_e32 v7, -1
	s_mov_b32 s47, 7
	s_movk_i32 s46, 0x80
	s_mov_b32 s38, 0x200000
	s_mov_b32 s39, 0x20000
	s_lshl_b32 s16, s24, 1
	s_and_b32 s16, s16, 14
	s_mov_b32 s17, 0
	s_waitcnt lgkmcnt(0)
	s_add_u32 s28, s4, 0x18800000
	s_addc_u32 s29, s5, 0
	s_add_u32 s30, s4, 0x18000000
	s_addc_u32 s31, s5, 0

.Lv_reprime:
	s_lshl_b32 s2, s20, 8
	s_add_u32 s2, s28, s2
	s_addc_u32 s3, s29, 0
	global_load_dwordx4 v[8:11], v2, s[2:3]
	global_load_dwordx4 v[12:15], v2, s[2:3] offset:16
	s_lshl_b32 s2, s20, 8
	s_add_u32 s2, s30, s2
	s_addc_u32 s3, s31, 0
	global_load_dwordx4 v[24:27], v2, s[2:3]
	global_load_dwordx4 v[28:31], v2, s[2:3] offset:16
	s_lshl_b32 s2, s21, 8
	s_add_u32 s2, s28, s2
	s_addc_u32 s3, s29, 0
	global_load_dwordx4 v[16:19], v2, s[2:3]
	global_load_dwordx4 v[20:23], v2, s[2:3] offset:16
	s_waitcnt vmcnt(0)
	v_mad_u32_u16 v112, v8, s46, v1
	buffer_load_dwordx4 v[48:51], v112, s[36:39], 0 offen
	v_mad_u32_u16 v113, v8, s46, v1 op_sel:[1,0,0,0]
	buffer_load_dwordx4 v[52:55], v113, s[36:39], 0 offen
	v_mad_u32_u16 v112, v9, s46, v1
	buffer_load_dwordx4 v[56:59], v112, s[36:39], 0 offen
	v_mad_u32_u16 v113, v9, s46, v1 op_sel:[1,0,0,0]
	buffer_load_dwordx4 v[60:63], v113, s[36:39], 0 offen
	v_mad_u32_u16 v112, v10, s46, v1
	buffer_load_dwordx4 v[64:67], v112, s[36:39], 0 offen
	v_mad_u32_u16 v113, v10, s46, v1 op_sel:[1,0,0,0]
	buffer_load_dwordx4 v[68:71], v113, s[36:39], 0 offen
	v_mad_u32_u16 v112, v11, s46, v1
	buffer_load_dwordx4 v[72:75], v112, s[36:39], 0 offen
	v_mad_u32_u16 v113, v11, s46, v1 op_sel:[1,0,0,0]
	buffer_load_dwordx4 v[76:79], v113, s[36:39], 0 offen
	v_mad_u32_u16 v112, v12, s46, v1
	buffer_load_dwordx4 v[80:83], v112, s[36:39], 0 offen
	v_mad_u32_u16 v113, v12, s46, v1 op_sel:[1,0,0,0]
	buffer_load_dwordx4 v[84:87], v113, s[36:39], 0 offen
	v_mad_u32_u16 v112, v13, s46, v1
	buffer_load_dwordx4 v[88:91], v112, s[36:39], 0 offen
	v_mad_u32_u16 v113, v13, s46, v1 op_sel:[1,0,0,0]
	buffer_load_dwordx4 v[92:95], v113, s[36:39], 0 offen
	v_mad_u32_u16 v112, v14, s46, v1
	buffer_load_dwordx4 v[96:99], v112, s[36:39], 0 offen
	v_mad_u32_u16 v113, v14, s46, v1 op_sel:[1,0,0,0]
	buffer_load_dwordx4 v[100:103], v113, s[36:39], 0 offen
	v_mad_u32_u16 v112, v15, s46, v1
	buffer_load_dwordx4 v[104:107], v112, s[36:39], 0 offen
	v_mad_u32_u16 v113, v15, s46, v1 op_sel:[1,0,0,0]
	buffer_load_dwordx4 v[108:111], v113, s[36:39], 0 offen
	global_load_dword v252, v5, s[28:29]

.Lv_got_l0:
	s_lshl_b32 s2, s22, 8
	s_add_u32 s2, s28, s2
	s_addc_u32 s3, s29, 0
	global_load_dwordx4 v[8:11], v2, s[2:3]
	global_load_dwordx4 v[12:15], v2, s[2:3] offset:16
	s_lshl_b32 s2, s21, 8
	s_add_u32 s2, s30, s2
	s_addc_u32 s3, s31, 0
	global_load_dwordx4 v[32:35], v2, s[2:3]
	global_load_dwordx4 v[36:39], v2, s[2:3] offset:16
	s_waitcnt vmcnt(20)
	v_cvt_pk_f32_fp8_e32 v[116:117], v48
	v_cvt_pk_f32_fp8_sdwa v[118:119], v48 src0_sel:WORD_1
	v_cvt_pk_f32_fp8_e32 v[120:121], v49
	v_cvt_pk_f32_fp8_sdwa v[122:123], v49 src0_sel:WORD_1
	v_cvt_pk_f32_fp8_e32 v[124:125], v50
	v_cvt_pk_f32_fp8_sdwa v[126:127], v50 src0_sel:WORD_1
	v_cvt_pk_f32_fp8_e32 v[128:129], v51
	v_cvt_pk_f32_fp8_sdwa v[130:131], v51 src0_sel:WORD_1
	v_lshlrev_b32_e32 v148, 16, v24
	v_mad_u32_u16 v112, v16, s46, v1
	buffer_load_dwordx4 v[48:51], v112, s[36:39], 0 offen
	v_pk_mul_f32 v[152:153], v[148:149], v[116:117] op_sel_hi:[0,1]
	v_pk_mul_f32 v[154:155], v[148:149], v[118:119] op_sel_hi:[0,1]
	v_pk_mul_f32 v[156:157], v[148:149], v[120:121] op_sel_hi:[0,1]
	v_pk_mul_f32 v[158:159], v[148:149], v[122:123] op_sel_hi:[0,1]
	v_pk_mul_f32 v[160:161], v[148:149], v[124:125] op_sel_hi:[0,1]
	v_pk_mul_f32 v[162:163], v[148:149], v[126:127] op_sel_hi:[0,1]
	v_pk_mul_f32 v[164:165], v[148:149], v[128:129] op_sel_hi:[0,1]
	v_pk_mul_f32 v[166:167], v[148:149], v[130:131] op_sel_hi:[0,1]
	s_waitcnt vmcnt(20)
	v_cvt_pk_f32_fp8_e32 v[132:133], v52
	v_cvt_pk_f32_fp8_sdwa v[134:135], v52 src0_sel:WORD_1
	v_cvt_pk_f32_fp8_e32 v[136:137], v53
	v_cvt_pk_f32_fp8_sdwa v[138:139], v53 src0_sel:WORD_1
	v_cvt_pk_f32_fp8_e32 v[140:141], v54
	v_cvt_pk_f32_fp8_sdwa v[142:143], v54 src0_sel:WORD_1
	v_cvt_pk_f32_fp8_e32 v[144:145], v55
	v_cvt_pk_f32_fp8_sdwa v[146:147], v55 src0_sel:WORD_1
	v_and_b32_e32 v150, 0xffff0000, v24
	v_mad_u32_u16 v113, v16, s46, v1 op_sel:[1,0,0,0]
	buffer_load_dwordx4 v[52:55], v113, s[36:39], 0 offen
	v_pk_fma_f32 v[152:153], v[150:151], v[132:133], v[152:153] op_sel_hi:[0,1,1]
	v_pk_fma_f32 v[154:155], v[150:151], v[134:135], v[154:155] op_sel_hi:[0,1,1]
	v_pk_fma_f32 v[156:157], v[150:151], v[136:137], v[156:157] op_sel_hi:[0,1,1]
	v_pk_fma_f32 v[158:159], v[150:151], v[138:139], v[158:159] op_sel_hi:[0,1,1]
	v_pk_fma_f32 v[160:161], v[150:151], v[140:141], v[160:161] op_sel_hi:[0,1,1]
	v_pk_fma_f32 v[162:163], v[150:151], v[142:143], v[162:163] op_sel_hi:[0,1,1]
	v_pk_fma_f32 v[164:165], v[150:151], v[144:145], v[164:165] op_sel_hi:[0,1,1]
	v_pk_fma_f32 v[166:167], v[150:151], v[146:147], v[166:167] op_sel_hi:[0,1,1]
	s_waitcnt vmcnt(20)
	v_cvt_pk_f32_fp8_e32 v[116:117], v56
	v_cvt_pk_f32_fp8_sdwa v[118:119], v56 src0_sel:WORD_1
	v_cvt_pk_f32_fp8_e32 v[120:121], v57
	v_cvt_pk_f32_fp8_sdwa v[122:123], v57 src0_sel:WORD_1
	v_cvt_pk_f32_fp8_e32 v[124:125], v58
	v_cvt_pk_f32_fp8_sdwa v[126:127], v58 src0_sel:WORD_1
	v_cvt_pk_f32_fp8_e32 v[128:129], v59
	v_cvt_pk_f32_fp8_sdwa v[130:131], v59 src0_sel:WORD_1
	v_lshlrev_b32_e32 v148, 16, v25
	v_mad_u32_u16 v112, v17, s46, v1
	buffer_load_dwordx4 v[56:59], v112, s[36:39], 0 offen
	v_pk_fma_f32 v[152:153], v[148:149], v[116:117], v[152:153] op_sel_hi:[0,1,1]
	v_pk_fma_f32 v[154:155], v[148:149], v[118:119], v[154:155] op_sel_hi:[0,1,1]
	v_pk_fma_f32 v[156:157], v[148:149], v[120:121], v[156:157] op_sel_hi:[0,1,1]
	v_pk_fma_f32 v[158:159], v[148:149], v[122:123], v[158:159] op_sel_hi:[0,1,1]
	v_pk_fma_f32 v[160:161], v[148:149], v[124:125], v[160:161] op_sel_hi:[0,1,1]
	v_pk_fma_f32 v[162:163], v[148:149], v[126:127], v[162:163] op_sel_hi:[0,1,1]
	v_pk_fma_f32 v[164:165], v[148:149], v[128:129], v[164:165] op_sel_hi:[0,1,1]
	v_pk_fma_f32 v[166:167], v[148:149], v[130:131], v[166:167] op_sel_hi:[0,1,1]
	s_waitcnt vmcnt(20)
	v_cvt_pk_f32_fp8_e32 v[132:133], v60
	v_cvt_pk_f32_fp8_sdwa v[134:135], v60 src0_sel:WORD_1
	v_cvt_pk_f32_fp8_e32 v[136:137], v61
	v_cvt_pk_f32_fp8_sdwa v[138:139], v61 src0_sel:WORD_1
	v_cvt_pk_f32_fp8_e32 v[140:141], v62
	v_cvt_pk_f32_fp8_sdwa v[142:143], v62 src0_sel:WORD_1
	v_cvt_pk_f32_fp8_e32 v[144:145], v63
	v_cvt_pk_f32_fp8_sdwa v[146:147], v63 src0_sel:WORD_1
	v_and_b32_e32 v150, 0xffff0000, v25
	v_mad_u32_u16 v113, v17, s46, v1 op_sel:[1,0,0,0]
	buffer_load_dwordx4 v[60:63], v113, s[36:39], 0 offen
	v_pk_fma_f32 v[152:153], v[150:151], v[132:133], v[152:153] op_sel_hi:[0,1,1]
	v_pk_fma_f32 v[154:155], v[150:151], v[134:135], v[154:155] op_sel_hi:[0,1,1]
	v_pk_fma_f32 v[156:157], v[150:151], v[136:137], v[156:157] op_sel_hi:[0,1,1]
	v_pk_fma_f32 v[158:159], v[150:151], v[138:139], v[158:159] op_sel_hi:[0,1,1]
	v_pk_fma_f32 v[160:161], v[150:151], v[140:141], v[160:161] op_sel_hi:[0,1,1]
	v_pk_fma_f32 v[162:163], v[150:151], v[142:143], v[162:163] op_sel_hi:[0,1,1]
	v_pk_fma_f32 v[164:165], v[150:151], v[144:145], v[164:165] op_sel_hi:[0,1,1]
	v_pk_fma_f32 v[166:167], v[150:151], v[146:147], v[166:167] op_sel_hi:[0,1,1]
	s_waitcnt vmcnt(20)
	v_cvt_pk_f32_fp8_e32 v[116:117], v64
	v_cvt_pk_f32_fp8_sdwa v[118:119], v64 src0_sel:WORD_1
	v_cvt_pk_f32_fp8_e32 v[120:121], v65
	v_cvt_pk_f32_fp8_sdwa v[122:123], v65 src0_sel:WORD_1
	v_cvt_pk_f32_fp8_e32 v[124:125], v66
	v_cvt_pk_f32_fp8_sdwa v[126:127], v66 src0_sel:WORD_1
	v_cvt_pk_f32_fp8_e32 v[128:129], v67
	v_cvt_pk_f32_fp8_sdwa v[130:131], v67 src0_sel:WORD_1
	v_lshlrev_b32_e32 v148, 16, v26
	v_mad_u32_u16 v112, v18, s46, v1
	buffer_load_dwordx4 v[64:67], v112, s[36:39], 0 offen
	v_pk_fma_f32 v[152:153], v[148:149], v[116:117], v[152:153] op_sel_hi:[0,1,1]
	v_pk_fma_f32 v[154:155], v[148:149], v[118:119], v[154:155] op_sel_hi:[0,1,1]
	v_pk_fma_f32 v[156:157], v[148:149], v[120:121], v[156:157] op_sel_hi:[0,1,1]
	v_pk_fma_f32 v[158:159], v[148:149], v[122:123], v[158:159] op_sel_hi:[0,1,1]
	v_pk_fma_f32 v[160:161], v[148:149], v[124:125], v[160:161] op_sel_hi:[0,1,1]
	v_pk_fma_f32 v[162:163], v[148:149], v[126:127], v[162:163] op_sel_hi:[0,1,1]
	v_pk_fma_f32 v[164:165], v[148:149], v[128:129], v[164:165] op_sel_hi:[0,1,1]
	v_pk_fma_f32 v[166:167], v[148:149], v[130:131], v[166:167] op_sel_hi:[0,1,1]
	s_waitcnt vmcnt(20)
	v_cvt_pk_f32_fp8_e32 v[132:133], v68
	v_cvt_pk_f32_fp8_sdwa v[134:135], v68 src0_sel:WORD_1
	v_cvt_pk_f32_fp8_e32 v[136:137], v69
	v_cvt_pk_f32_fp8_sdwa v[138:139], v69 src0_sel:WORD_1
	v_cvt_pk_f32_fp8_e32 v[140:141], v70
	v_cvt_pk_f32_fp8_sdwa v[142:143], v70 src0_sel:WORD_1
	v_cvt_pk_f32_fp8_e32 v[144:145], v71
	v_cvt_pk_f32_fp8_sdwa v[146:147], v71 src0_sel:WORD_1
	v_and_b32_e32 v150, 0xffff0000, v26
	v_mad_u32_u16 v113, v18, s46, v1 op_sel:[1,0,0,0]
	buffer_load_dwordx4 v[68:71], v113, s[36:39], 0 offen
	v_pk_fma_f32 v[152:153], v[150:151], v[132:133], v[152:153] op_sel_hi:[0,1,1]
	v_pk_fma_f32 v[154:155], v[150:151], v[134:135], v[154:155] op_sel_hi:[0,1,1]
	v_pk_fma_f32 v[156:157], v[150:151], v[136:137], v[156:157] op_sel_hi:[0,1,1]
	v_pk_fma_f32 v[158:159], v[150:151], v[138:139], v[158:159] op_sel_hi:[0,1,1]
	v_pk_fma_f32 v[160:161], v[150:151], v[140:141], v[160:161] op_sel_hi:[0,1,1]
	v_pk_fma_f32 v[162:163], v[150:151], v[142:143], v[162:163] op_sel_hi:[0,1,1]
	v_pk_fma_f32 v[164:165], v[150:151], v[144:145], v[164:165] op_sel_hi:[0,1,1]
	v_pk_fma_f32 v[166:167], v[150:151], v[146:147], v[166:167] op_sel_hi:[0,1,1]
	s_waitcnt vmcnt(20)
	v_cvt_pk_f32_fp8_e32 v[116:117], v72
	v_cvt_pk_f32_fp8_sdwa v[118:119], v72 src0_sel:WORD_1
	v_cvt_pk_f32_fp8_e32 v[120:121], v73
	v_cvt_pk_f32_fp8_sdwa v[122:123], v73 src0_sel:WORD_1
	v_cvt_pk_f32_fp8_e32 v[124:125], v74
	v_cvt_pk_f32_fp8_sdwa v[126:127], v74 src0_sel:WORD_1
	v_cvt_pk_f32_fp8_e32 v[128:129], v75
	v_cvt_pk_f32_fp8_sdwa v[130:131], v75 src0_sel:WORD_1
	v_lshlrev_b32_e32 v148, 16, v27
	v_mad_u32_u16 v112, v19, s46, v1
	buffer_load_dwordx4 v[72:75], v112, s[36:39], 0 offen
	v_pk_fma_f32 v[152:153], v[148:149], v[116:117], v[152:153] op_sel_hi:[0,1,1]
	v_pk_fma_f32 v[154:155], v[148:149], v[118:119], v[154:155] op_sel_hi:[0,1,1]
	v_pk_fma_f32 v[156:157], v[148:149], v[120:121], v[156:157] op_sel_hi:[0,1,1]
	v_pk_fma_f32 v[158:159], v[148:149], v[122:123], v[158:159] op_sel_hi:[0,1,1]
	v_pk_fma_f32 v[160:161], v[148:149], v[124:125], v[160:161] op_sel_hi:[0,1,1]
	v_pk_fma_f32 v[162:163], v[148:149], v[126:127], v[162:163] op_sel_hi:[0,1,1]
	v_pk_fma_f32 v[164:165], v[148:149], v[128:129], v[164:165] op_sel_hi:[0,1,1]
	v_pk_fma_f32 v[166:167], v[148:149], v[130:131], v[166:167] op_sel_hi:[0,1,1]
	s_waitcnt vmcnt(20)
	v_cvt_pk_f32_fp8_e32 v[132:133], v76
	v_cvt_pk_f32_fp8_sdwa v[134:135], v76 src0_sel:WORD_1
	v_cvt_pk_f32_fp8_e32 v[136:137], v77
	v_cvt_pk_f32_fp8_sdwa v[138:139], v77 src0_sel:WORD_1
	v_cvt_pk_f32_fp8_e32 v[140:141], v78
	v_cvt_pk_f32_fp8_sdwa v[142:143], v78 src0_sel:WORD_1
	v_cvt_pk_f32_fp8_e32 v[144:145], v79
	v_cvt_pk_f32_fp8_sdwa v[146:147], v79 src0_sel:WORD_1
	v_and_b32_e32 v150, 0xffff0000, v27
	v_mad_u32_u16 v113, v19, s46, v1 op_sel:[1,0,0,0]
	buffer_load_dwordx4 v[76:79], v113, s[36:39], 0 offen
	v_pk_fma_f32 v[152:153], v[150:151], v[132:133], v[152:153] op_sel_hi:[0,1,1]
	v_pk_fma_f32 v[154:155], v[150:151], v[134:135], v[154:155] op_sel_hi:[0,1,1]
	v_pk_fma_f32 v[156:157], v[150:151], v[136:137], v[156:157] op_sel_hi:[0,1,1]
	v_pk_fma_f32 v[158:159], v[150:151], v[138:139], v[158:159] op_sel_hi:[0,1,1]
	v_pk_fma_f32 v[160:161], v[150:151], v[140:141], v[160:161] op_sel_hi:[0,1,1]
	v_pk_fma_f32 v[162:163], v[150:151], v[142:143], v[162:163] op_sel_hi:[0,1,1]
	v_pk_fma_f32 v[164:165], v[150:151], v[144:145], v[164:165] op_sel_hi:[0,1,1]
	v_pk_fma_f32 v[166:167], v[150:151], v[146:147], v[166:167] op_sel_hi:[0,1,1]
	s_waitcnt vmcnt(20)
	v_cvt_pk_f32_fp8_e32 v[116:117], v80
	v_cvt_pk_f32_fp8_sdwa v[118:119], v80 src0_sel:WORD_1
	v_cvt_pk_f32_fp8_e32 v[120:121], v81
	v_cvt_pk_f32_fp8_sdwa v[122:123], v81 src0_sel:WORD_1
	v_cvt_pk_f32_fp8_e32 v[124:125], v82
	v_cvt_pk_f32_fp8_sdwa v[126:127], v82 src0_sel:WORD_1
	v_cvt_pk_f32_fp8_e32 v[128:129], v83
	v_cvt_pk_f32_fp8_sdwa v[130:131], v83 src0_sel:WORD_1
	v_lshlrev_b32_e32 v148, 16, v28
	v_mad_u32_u16 v112, v20, s46, v1
	buffer_load_dwordx4 v[80:83], v112, s[36:39], 0 offen
	v_pk_fma_f32 v[152:153], v[148:149], v[116:117], v[152:153] op_sel_hi:[0,1,1]
	v_pk_fma_f32 v[154:155], v[148:149], v[118:119], v[154:155] op_sel_hi:[0,1,1]
	v_pk_fma_f32 v[156:157], v[148:149], v[120:121], v[156:157] op_sel_hi:[0,1,1]
	v_pk_fma_f32 v[158:159], v[148:149], v[122:123], v[158:159] op_sel_hi:[0,1,1]
	v_pk_fma_f32 v[160:161], v[148:149], v[124:125], v[160:161] op_sel_hi:[0,1,1]
	v_pk_fma_f32 v[162:163], v[148:149], v[126:127], v[162:163] op_sel_hi:[0,1,1]
	v_pk_fma_f32 v[164:165], v[148:149], v[128:129], v[164:165] op_sel_hi:[0,1,1]
	v_pk_fma_f32 v[166:167], v[148:149], v[130:131], v[166:167] op_sel_hi:[0,1,1]
	s_waitcnt vmcnt(20)
	v_cvt_pk_f32_fp8_e32 v[132:133], v84
	v_cvt_pk_f32_fp8_sdwa v[134:135], v84 src0_sel:WORD_1
	v_cvt_pk_f32_fp8_e32 v[136:137], v85
	v_cvt_pk_f32_fp8_sdwa v[138:139], v85 src0_sel:WORD_1
	v_cvt_pk_f32_fp8_e32 v[140:141], v86
	v_cvt_pk_f32_fp8_sdwa v[142:143], v86 src0_sel:WORD_1
	v_cvt_pk_f32_fp8_e32 v[144:145], v87
	v_cvt_pk_f32_fp8_sdwa v[146:147], v87 src0_sel:WORD_1
	v_and_b32_e32 v150, 0xffff0000, v28
	v_mad_u32_u16 v113, v20, s46, v1 op_sel:[1,0,0,0]
	buffer_load_dwordx4 v[84:87], v113, s[36:39], 0 offen
	v_pk_fma_f32 v[152:153], v[150:151], v[132:133], v[152:153] op_sel_hi:[0,1,1]
	v_pk_fma_f32 v[154:155], v[150:151], v[134:135], v[154:155] op_sel_hi:[0,1,1]
	v_pk_fma_f32 v[156:157], v[150:151], v[136:137], v[156:157] op_sel_hi:[0,1,1]
	v_pk_fma_f32 v[158:159], v[150:151], v[138:139], v[158:159] op_sel_hi:[0,1,1]
	v_pk_fma_f32 v[160:161], v[150:151], v[140:141], v[160:161] op_sel_hi:[0,1,1]
	v_pk_fma_f32 v[162:163], v[150:151], v[142:143], v[162:163] op_sel_hi:[0,1,1]
	v_pk_fma_f32 v[164:165], v[150:151], v[144:145], v[164:165] op_sel_hi:[0,1,1]
	v_pk_fma_f32 v[166:167], v[150:151], v[146:147], v[166:167] op_sel_hi:[0,1,1]
	s_waitcnt vmcnt(20)
	v_cvt_pk_f32_fp8_e32 v[116:117], v88
	v_cvt_pk_f32_fp8_sdwa v[118:119], v88 src0_sel:WORD_1
	v_cvt_pk_f32_fp8_e32 v[120:121], v89
	v_cvt_pk_f32_fp8_sdwa v[122:123], v89 src0_sel:WORD_1
	v_cvt_pk_f32_fp8_e32 v[124:125], v90
	v_cvt_pk_f32_fp8_sdwa v[126:127], v90 src0_sel:WORD_1
	v_cvt_pk_f32_fp8_e32 v[128:129], v91
	v_cvt_pk_f32_fp8_sdwa v[130:131], v91 src0_sel:WORD_1
	v_lshlrev_b32_e32 v148, 16, v29
	v_mad_u32_u16 v112, v21, s46, v1
	buffer_load_dwordx4 v[88:91], v112, s[36:39], 0 offen
	v_pk_fma_f32 v[152:153], v[148:149], v[116:117], v[152:153] op_sel_hi:[0,1,1]
	v_pk_fma_f32 v[154:155], v[148:149], v[118:119], v[154:155] op_sel_hi:[0,1,1]
	v_pk_fma_f32 v[156:157], v[148:149], v[120:121], v[156:157] op_sel_hi:[0,1,1]
	v_pk_fma_f32 v[158:159], v[148:149], v[122:123], v[158:159] op_sel_hi:[0,1,1]
	v_pk_fma_f32 v[160:161], v[148:149], v[124:125], v[160:161] op_sel_hi:[0,1,1]
	v_pk_fma_f32 v[162:163], v[148:149], v[126:127], v[162:163] op_sel_hi:[0,1,1]
	v_pk_fma_f32 v[164:165], v[148:149], v[128:129], v[164:165] op_sel_hi:[0,1,1]
	v_pk_fma_f32 v[166:167], v[148:149], v[130:131], v[166:167] op_sel_hi:[0,1,1]
	s_waitcnt vmcnt(20)
	v_cvt_pk_f32_fp8_e32 v[132:133], v92
	v_cvt_pk_f32_fp8_sdwa v[134:135], v92 src0_sel:WORD_1
	v_cvt_pk_f32_fp8_e32 v[136:137], v93
	v_cvt_pk_f32_fp8_sdwa v[138:139], v93 src0_sel:WORD_1
	v_cvt_pk_f32_fp8_e32 v[140:141], v94
	v_cvt_pk_f32_fp8_sdwa v[142:143], v94 src0_sel:WORD_1
	v_cvt_pk_f32_fp8_e32 v[144:145], v95
	v_cvt_pk_f32_fp8_sdwa v[146:147], v95 src0_sel:WORD_1
	v_and_b32_e32 v150, 0xffff0000, v29
	v_mad_u32_u16 v113, v21, s46, v1 op_sel:[1,0,0,0]
	buffer_load_dwordx4 v[92:95], v113, s[36:39], 0 offen
	v_pk_fma_f32 v[152:153], v[150:151], v[132:133], v[152:153] op_sel_hi:[0,1,1]
	v_pk_fma_f32 v[154:155], v[150:151], v[134:135], v[154:155] op_sel_hi:[0,1,1]
	v_pk_fma_f32 v[156:157], v[150:151], v[136:137], v[156:157] op_sel_hi:[0,1,1]
	v_pk_fma_f32 v[158:159], v[150:151], v[138:139], v[158:159] op_sel_hi:[0,1,1]
	v_pk_fma_f32 v[160:161], v[150:151], v[140:141], v[160:161] op_sel_hi:[0,1,1]
	v_pk_fma_f32 v[162:163], v[150:151], v[142:143], v[162:163] op_sel_hi:[0,1,1]
	v_pk_fma_f32 v[164:165], v[150:151], v[144:145], v[164:165] op_sel_hi:[0,1,1]
	v_pk_fma_f32 v[166:167], v[150:151], v[146:147], v[166:167] op_sel_hi:[0,1,1]
	s_waitcnt vmcnt(20)
	v_cvt_pk_f32_fp8_e32 v[116:117], v96
	v_cvt_pk_f32_fp8_sdwa v[118:119], v96 src0_sel:WORD_1
	v_cvt_pk_f32_fp8_e32 v[120:121], v97
	v_cvt_pk_f32_fp8_sdwa v[122:123], v97 src0_sel:WORD_1
	v_cvt_pk_f32_fp8_e32 v[124:125], v98
	v_cvt_pk_f32_fp8_sdwa v[126:127], v98 src0_sel:WORD_1
	v_cvt_pk_f32_fp8_e32 v[128:129], v99
	v_cvt_pk_f32_fp8_sdwa v[130:131], v99 src0_sel:WORD_1
	v_lshlrev_b32_e32 v148, 16, v30
	v_mad_u32_u16 v112, v22, s46, v1
	buffer_load_dwordx4 v[96:99], v112, s[36:39], 0 offen
	v_pk_fma_f32 v[152:153], v[148:149], v[116:117], v[152:153] op_sel_hi:[0,1,1]
	v_pk_fma_f32 v[154:155], v[148:149], v[118:119], v[154:155] op_sel_hi:[0,1,1]
	v_pk_fma_f32 v[156:157], v[148:149], v[120:121], v[156:157] op_sel_hi:[0,1,1]
	v_pk_fma_f32 v[158:159], v[148:149], v[122:123], v[158:159] op_sel_hi:[0,1,1]
	v_pk_fma_f32 v[160:161], v[148:149], v[124:125], v[160:161] op_sel_hi:[0,1,1]
	v_pk_fma_f32 v[162:163], v[148:149], v[126:127], v[162:163] op_sel_hi:[0,1,1]
	v_pk_fma_f32 v[164:165], v[148:149], v[128:129], v[164:165] op_sel_hi:[0,1,1]
	v_pk_fma_f32 v[166:167], v[148:149], v[130:131], v[166:167] op_sel_hi:[0,1,1]
	s_waitcnt vmcnt(20)
	v_cvt_pk_f32_fp8_e32 v[132:133], v100
	v_cvt_pk_f32_fp8_sdwa v[134:135], v100 src0_sel:WORD_1
	v_cvt_pk_f32_fp8_e32 v[136:137], v101
	v_cvt_pk_f32_fp8_sdwa v[138:139], v101 src0_sel:WORD_1
	v_cvt_pk_f32_fp8_e32 v[140:141], v102
	v_cvt_pk_f32_fp8_sdwa v[142:143], v102 src0_sel:WORD_1
	v_cvt_pk_f32_fp8_e32 v[144:145], v103
	v_cvt_pk_f32_fp8_sdwa v[146:147], v103 src0_sel:WORD_1
	v_and_b32_e32 v150, 0xffff0000, v30
	v_mad_u32_u16 v113, v22, s46, v1 op_sel:[1,0,0,0]
	buffer_load_dwordx4 v[100:103], v113, s[36:39], 0 offen
	v_pk_fma_f32 v[152:153], v[150:151], v[132:133], v[152:153] op_sel_hi:[0,1,1]
	v_pk_fma_f32 v[154:155], v[150:151], v[134:135], v[154:155] op_sel_hi:[0,1,1]
	v_pk_fma_f32 v[156:157], v[150:151], v[136:137], v[156:157] op_sel_hi:[0,1,1]
	v_pk_fma_f32 v[158:159], v[150:151], v[138:139], v[158:159] op_sel_hi:[0,1,1]
	v_pk_fma_f32 v[160:161], v[150:151], v[140:141], v[160:161] op_sel_hi:[0,1,1]
	v_pk_fma_f32 v[162:163], v[150:151], v[142:143], v[162:163] op_sel_hi:[0,1,1]
	v_pk_fma_f32 v[164:165], v[150:151], v[144:145], v[164:165] op_sel_hi:[0,1,1]
	v_pk_fma_f32 v[166:167], v[150:151], v[146:147], v[166:167] op_sel_hi:[0,1,1]
	s_waitcnt vmcnt(20)
	v_cvt_pk_f32_fp8_e32 v[116:117], v104
	v_cvt_pk_f32_fp8_sdwa v[118:119], v104 src0_sel:WORD_1
	v_cvt_pk_f32_fp8_e32 v[120:121], v105
	v_cvt_pk_f32_fp8_sdwa v[122:123], v105 src0_sel:WORD_1
	v_cvt_pk_f32_fp8_e32 v[124:125], v106
	v_cvt_pk_f32_fp8_sdwa v[126:127], v106 src0_sel:WORD_1
	v_cvt_pk_f32_fp8_e32 v[128:129], v107
	v_cvt_pk_f32_fp8_sdwa v[130:131], v107 src0_sel:WORD_1
	v_lshlrev_b32_e32 v148, 16, v31
	v_mad_u32_u16 v112, v23, s46, v1
	buffer_load_dwordx4 v[104:107], v112, s[36:39], 0 offen
	v_pk_fma_f32 v[152:153], v[148:149], v[116:117], v[152:153] op_sel_hi:[0,1,1]
	v_pk_fma_f32 v[154:155], v[148:149], v[118:119], v[154:155] op_sel_hi:[0,1,1]
	v_pk_fma_f32 v[156:157], v[148:149], v[120:121], v[156:157] op_sel_hi:[0,1,1]
	v_pk_fma_f32 v[158:159], v[148:149], v[122:123], v[158:159] op_sel_hi:[0,1,1]
	v_pk_fma_f32 v[160:161], v[148:149], v[124:125], v[160:161] op_sel_hi:[0,1,1]
	v_pk_fma_f32 v[162:163], v[148:149], v[126:127], v[162:163] op_sel_hi:[0,1,1]
	v_pk_fma_f32 v[164:165], v[148:149], v[128:129], v[164:165] op_sel_hi:[0,1,1]
	v_pk_fma_f32 v[166:167], v[148:149], v[130:131], v[166:167] op_sel_hi:[0,1,1]
	s_waitcnt vmcnt(20)
	v_cvt_pk_f32_fp8_e32 v[132:133], v108
	v_cvt_pk_f32_fp8_sdwa v[134:135], v108 src0_sel:WORD_1
	v_cvt_pk_f32_fp8_e32 v[136:137], v109
	v_cvt_pk_f32_fp8_sdwa v[138:139], v109 src0_sel:WORD_1
	v_cvt_pk_f32_fp8_e32 v[140:141], v110
	v_cvt_pk_f32_fp8_sdwa v[142:143], v110 src0_sel:WORD_1
	v_cvt_pk_f32_fp8_e32 v[144:145], v111
	v_cvt_pk_f32_fp8_sdwa v[146:147], v111 src0_sel:WORD_1
	v_and_b32_e32 v150, 0xffff0000, v31
	v_mad_u32_u16 v113, v23, s46, v1 op_sel:[1,0,0,0]
	buffer_load_dwordx4 v[108:111], v113, s[36:39], 0 offen
	v_pk_fma_f32 v[152:153], v[150:151], v[132:133], v[152:153] op_sel_hi:[0,1,1]
	v_pk_fma_f32 v[154:155], v[150:151], v[134:135], v[154:155] op_sel_hi:[0,1,1]
	v_pk_fma_f32 v[156:157], v[150:151], v[136:137], v[156:157] op_sel_hi:[0,1,1]
	v_pk_fma_f32 v[158:159], v[150:151], v[138:139], v[158:159] op_sel_hi:[0,1,1]
	v_pk_fma_f32 v[160:161], v[150:151], v[140:141], v[160:161] op_sel_hi:[0,1,1]
	v_pk_fma_f32 v[162:163], v[150:151], v[142:143], v[162:163] op_sel_hi:[0,1,1]
	v_pk_fma_f32 v[164:165], v[150:151], v[144:145], v[164:165] op_sel_hi:[0,1,1]
	v_pk_fma_f32 v[166:167], v[150:151], v[146:147], v[166:167] op_sel_hi:[0,1,1]
	s_nop 1
	v_permlane32_swap_b32_e32 v152, v160
	v_permlane32_swap_b32_e32 v153, v161
	v_permlane32_swap_b32_e32 v154, v162
	v_permlane32_swap_b32_e32 v155, v163
	v_permlane32_swap_b32_e32 v156, v164
	v_permlane32_swap_b32_e32 v157, v165
	v_permlane32_swap_b32_e32 v158, v166
	v_permlane32_swap_b32_e32 v159, v167
	v_add_f32_e32 v168, v152, v160
	v_add_f32_e32 v169, v153, v161
	v_add_f32_e32 v170, v154, v162
	v_add_f32_e32 v171, v155, v163
	v_add_f32_e32 v172, v156, v164
	v_add_f32_e32 v173, v157, v165
	v_add_f32_e32 v174, v158, v166
	v_add_f32_e32 v175, v159, v167
	s_nop 1
	v_permlane16_swap_b32_e32 v168, v172
	v_permlane16_swap_b32_e32 v169, v173
	v_permlane16_swap_b32_e32 v170, v174
	v_permlane16_swap_b32_e32 v171, v175
	v_add_f32_e32 v176, v168, v172
	v_add_f32_e32 v177, v169, v173
	v_add_f32_e32 v178, v170, v174
	v_add_f32_e32 v179, v171, v175
	v_cndmask_b32_e64 v180, v176, v178, s[44:45]
	v_cndmask_b32_e64 v181, v177, v179, s[44:45]
	v_cndmask_b32_e64 v182, v178, v176, s[44:45]
	v_cndmask_b32_e64 v183, v179, v177, s[44:45]
	s_nop 0
	v_add_f32_dpp v184, v180, v182 row_ror:8 row_mask:0xf bank_mask:0xf
	v_add_f32_dpp v185, v181, v183 row_ror:8 row_mask:0xf bank_mask:0xf
	v_cvt_pk_bf16_f32 v188, v184, v185
	s_lshl_b32 s2, s20, 12
	s_add_u32 s2, s34, s2
	s_addc_u32 s3, s35, 0
	global_store_dword v3, v188, s[2:3]
	s_mov_b32 s20, s21
	s_mov_b32 s48, s49
	s_mov_b32 s21, s22
	s_mov_b32 s49, s50
	s_cmp_eq_u32 s48, 0
	s_cbranch_scc1 .Lv_drain
	s_cmp_lg_u32 s26, 32
	s_cbranch_scc1 .Lv_norot_l1
	v_readfirstlane_b32 s23, v6
	s_mov_b64 exec, 1
	global_atomic_inc v6, v5, v7, s[6:7] sc0
	s_mov_b64 exec, -1
	s_mov_b32 s26, 0

.Lv_got_l1:
	s_lshl_b32 s2, s22, 8
	s_add_u32 s2, s28, s2
	s_addc_u32 s3, s29, 0
	global_load_dwordx4 v[16:19], v2, s[2:3]
	global_load_dwordx4 v[20:23], v2, s[2:3] offset:16
	s_lshl_b32 s2, s21, 8
	s_add_u32 s2, s30, s2
	s_addc_u32 s3, s31, 0
	global_load_dwordx4 v[24:27], v2, s[2:3]
	global_load_dwordx4 v[28:31], v2, s[2:3] offset:16
	s_waitcnt vmcnt(20)
	v_cvt_pk_f32_fp8_e32 v[116:117], v48
	v_cvt_pk_f32_fp8_sdwa v[118:119], v48 src0_sel:WORD_1
	v_cvt_pk_f32_fp8_e32 v[120:121], v49
	v_cvt_pk_f32_fp8_sdwa v[122:123], v49 src0_sel:WORD_1
	v_cvt_pk_f32_fp8_e32 v[124:125], v50
	v_cvt_pk_f32_fp8_sdwa v[126:127], v50 src0_sel:WORD_1
	v_cvt_pk_f32_fp8_e32 v[128:129], v51
	v_cvt_pk_f32_fp8_sdwa v[130:131], v51 src0_sel:WORD_1
	v_lshlrev_b32_e32 v148, 16, v32
	v_mad_u32_u16 v112, v8, s46, v1
	buffer_load_dwordx4 v[48:51], v112, s[36:39], 0 offen
	v_pk_mul_f32 v[152:153], v[148:149], v[116:117] op_sel_hi:[0,1]
	v_pk_mul_f32 v[154:155], v[148:149], v[118:119] op_sel_hi:[0,1]
	v_pk_mul_f32 v[156:157], v[148:149], v[120:121] op_sel_hi:[0,1]
	v_pk_mul_f32 v[158:159], v[148:149], v[122:123] op_sel_hi:[0,1]
	v_pk_mul_f32 v[160:161], v[148:149], v[124:125] op_sel_hi:[0,1]
	v_pk_mul_f32 v[162:163], v[148:149], v[126:127] op_sel_hi:[0,1]
	v_pk_mul_f32 v[164:165], v[148:149], v[128:129] op_sel_hi:[0,1]
	v_pk_mul_f32 v[166:167], v[148:149], v[130:131] op_sel_hi:[0,1]
	s_waitcnt vmcnt(20)
	v_cvt_pk_f32_fp8_e32 v[132:133], v52
	v_cvt_pk_f32_fp8_sdwa v[134:135], v52 src0_sel:WORD_1
	v_cvt_pk_f32_fp8_e32 v[136:137], v53
	v_cvt_pk_f32_fp8_sdwa v[138:139], v53 src0_sel:WORD_1
	v_cvt_pk_f32_fp8_e32 v[140:141], v54
	v_cvt_pk_f32_fp8_sdwa v[142:143], v54 src0_sel:WORD_1
	v_cvt_pk_f32_fp8_e32 v[144:145], v55
	v_cvt_pk_f32_fp8_sdwa v[146:147], v55 src0_sel:WORD_1
	v_and_b32_e32 v150, 0xffff0000, v32
	v_mad_u32_u16 v113, v8, s46, v1 op_sel:[1,0,0,0]
	buffer_load_dwordx4 v[52:55], v113, s[36:39], 0 offen
	v_pk_fma_f32 v[152:153], v[150:151], v[132:133], v[152:153] op_sel_hi:[0,1,1]
	v_pk_fma_f32 v[154:155], v[150:151], v[134:135], v[154:155] op_sel_hi:[0,1,1]
	v_pk_fma_f32 v[156:157], v[150:151], v[136:137], v[156:157] op_sel_hi:[0,1,1]
	v_pk_fma_f32 v[158:159], v[150:151], v[138:139], v[158:159] op_sel_hi:[0,1,1]
	v_pk_fma_f32 v[160:161], v[150:151], v[140:141], v[160:161] op_sel_hi:[0,1,1]
	v_pk_fma_f32 v[162:163], v[150:151], v[142:143], v[162:163] op_sel_hi:[0,1,1]
	v_pk_fma_f32 v[164:165], v[150:151], v[144:145], v[164:165] op_sel_hi:[0,1,1]
	v_pk_fma_f32 v[166:167], v[150:151], v[146:147], v[166:167] op_sel_hi:[0,1,1]
	s_waitcnt vmcnt(20)
	v_cvt_pk_f32_fp8_e32 v[116:117], v56
	v_cvt_pk_f32_fp8_sdwa v[118:119], v56 src0_sel:WORD_1
	v_cvt_pk_f32_fp8_e32 v[120:121], v57
	v_cvt_pk_f32_fp8_sdwa v[122:123], v57 src0_sel:WORD_1
	v_cvt_pk_f32_fp8_e32 v[124:125], v58
	v_cvt_pk_f32_fp8_sdwa v[126:127], v58 src0_sel:WORD_1
	v_cvt_pk_f32_fp8_e32 v[128:129], v59
	v_cvt_pk_f32_fp8_sdwa v[130:131], v59 src0_sel:WORD_1
	v_lshlrev_b32_e32 v148, 16, v33
	v_mad_u32_u16 v112, v9, s46, v1
	buffer_load_dwordx4 v[56:59], v112, s[36:39], 0 offen
	v_pk_fma_f32 v[152:153], v[148:149], v[116:117], v[152:153] op_sel_hi:[0,1,1]
	v_pk_fma_f32 v[154:155], v[148:149], v[118:119], v[154:155] op_sel_hi:[0,1,1]
	v_pk_fma_f32 v[156:157], v[148:149], v[120:121], v[156:157] op_sel_hi:[0,1,1]
	v_pk_fma_f32 v[158:159], v[148:149], v[122:123], v[158:159] op_sel_hi:[0,1,1]
	v_pk_fma_f32 v[160:161], v[148:149], v[124:125], v[160:161] op_sel_hi:[0,1,1]
	v_pk_fma_f32 v[162:163], v[148:149], v[126:127], v[162:163] op_sel_hi:[0,1,1]
	v_pk_fma_f32 v[164:165], v[148:149], v[128:129], v[164:165] op_sel_hi:[0,1,1]
	v_pk_fma_f32 v[166:167], v[148:149], v[130:131], v[166:167] op_sel_hi:[0,1,1]
	s_waitcnt vmcnt(20)
	v_cvt_pk_f32_fp8_e32 v[132:133], v60
	v_cvt_pk_f32_fp8_sdwa v[134:135], v60 src0_sel:WORD_1
	v_cvt_pk_f32_fp8_e32 v[136:137], v61
	v_cvt_pk_f32_fp8_sdwa v[138:139], v61 src0_sel:WORD_1
	v_cvt_pk_f32_fp8_e32 v[140:141], v62
	v_cvt_pk_f32_fp8_sdwa v[142:143], v62 src0_sel:WORD_1
	v_cvt_pk_f32_fp8_e32 v[144:145], v63
	v_cvt_pk_f32_fp8_sdwa v[146:147], v63 src0_sel:WORD_1
	v_and_b32_e32 v150, 0xffff0000, v33
	v_mad_u32_u16 v113, v9, s46, v1 op_sel:[1,0,0,0]
	buffer_load_dwordx4 v[60:63], v113, s[36:39], 0 offen
	v_pk_fma_f32 v[152:153], v[150:151], v[132:133], v[152:153] op_sel_hi:[0,1,1]
	v_pk_fma_f32 v[154:155], v[150:151], v[134:135], v[154:155] op_sel_hi:[0,1,1]
	v_pk_fma_f32 v[156:157], v[150:151], v[136:137], v[156:157] op_sel_hi:[0,1,1]
	v_pk_fma_f32 v[158:159], v[150:151], v[138:139], v[158:159] op_sel_hi:[0,1,1]
	v_pk_fma_f32 v[160:161], v[150:151], v[140:141], v[160:161] op_sel_hi:[0,1,1]
	v_pk_fma_f32 v[162:163], v[150:151], v[142:143], v[162:163] op_sel_hi:[0,1,1]
	v_pk_fma_f32 v[164:165], v[150:151], v[144:145], v[164:165] op_sel_hi:[0,1,1]
	v_pk_fma_f32 v[166:167], v[150:151], v[146:147], v[166:167] op_sel_hi:[0,1,1]
	s_waitcnt vmcnt(20)
	v_cvt_pk_f32_fp8_e32 v[116:117], v64
	v_cvt_pk_f32_fp8_sdwa v[118:119], v64 src0_sel:WORD_1
	v_cvt_pk_f32_fp8_e32 v[120:121], v65
	v_cvt_pk_f32_fp8_sdwa v[122:123], v65 src0_sel:WORD_1
	v_cvt_pk_f32_fp8_e32 v[124:125], v66
	v_cvt_pk_f32_fp8_sdwa v[126:127], v66 src0_sel:WORD_1
	v_cvt_pk_f32_fp8_e32 v[128:129], v67
	v_cvt_pk_f32_fp8_sdwa v[130:131], v67 src0_sel:WORD_1
	v_lshlrev_b32_e32 v148, 16, v34
	v_mad_u32_u16 v112, v10, s46, v1
	buffer_load_dwordx4 v[64:67], v112, s[36:39], 0 offen
	v_pk_fma_f32 v[152:153], v[148:149], v[116:117], v[152:153] op_sel_hi:[0,1,1]
	v_pk_fma_f32 v[154:155], v[148:149], v[118:119], v[154:155] op_sel_hi:[0,1,1]
	v_pk_fma_f32 v[156:157], v[148:149], v[120:121], v[156:157] op_sel_hi:[0,1,1]
	v_pk_fma_f32 v[158:159], v[148:149], v[122:123], v[158:159] op_sel_hi:[0,1,1]
	v_pk_fma_f32 v[160:161], v[148:149], v[124:125], v[160:161] op_sel_hi:[0,1,1]
	v_pk_fma_f32 v[162:163], v[148:149], v[126:127], v[162:163] op_sel_hi:[0,1,1]
	v_pk_fma_f32 v[164:165], v[148:149], v[128:129], v[164:165] op_sel_hi:[0,1,1]
	v_pk_fma_f32 v[166:167], v[148:149], v[130:131], v[166:167] op_sel_hi:[0,1,1]
	s_waitcnt vmcnt(20)
	v_cvt_pk_f32_fp8_e32 v[132:133], v68
	v_cvt_pk_f32_fp8_sdwa v[134:135], v68 src0_sel:WORD_1
	v_cvt_pk_f32_fp8_e32 v[136:137], v69
	v_cvt_pk_f32_fp8_sdwa v[138:139], v69 src0_sel:WORD_1
	v_cvt_pk_f32_fp8_e32 v[140:141], v70
	v_cvt_pk_f32_fp8_sdwa v[142:143], v70 src0_sel:WORD_1
	v_cvt_pk_f32_fp8_e32 v[144:145], v71
	v_cvt_pk_f32_fp8_sdwa v[146:147], v71 src0_sel:WORD_1
	v_and_b32_e32 v150, 0xffff0000, v34
	v_mad_u32_u16 v113, v10, s46, v1 op_sel:[1,0,0,0]
	buffer_load_dwordx4 v[68:71], v113, s[36:39], 0 offen
	v_pk_fma_f32 v[152:153], v[150:151], v[132:133], v[152:153] op_sel_hi:[0,1,1]
	v_pk_fma_f32 v[154:155], v[150:151], v[134:135], v[154:155] op_sel_hi:[0,1,1]
	v_pk_fma_f32 v[156:157], v[150:151], v[136:137], v[156:157] op_sel_hi:[0,1,1]
	v_pk_fma_f32 v[158:159], v[150:151], v[138:139], v[158:159] op_sel_hi:[0,1,1]
	v_pk_fma_f32 v[160:161], v[150:151], v[140:141], v[160:161] op_sel_hi:[0,1,1]
	v_pk_fma_f32 v[162:163], v[150:151], v[142:143], v[162:163] op_sel_hi:[0,1,1]
	v_pk_fma_f32 v[164:165], v[150:151], v[144:145], v[164:165] op_sel_hi:[0,1,1]
	v_pk_fma_f32 v[166:167], v[150:151], v[146:147], v[166:167] op_sel_hi:[0,1,1]
	s_waitcnt vmcnt(20)
	v_cvt_pk_f32_fp8_e32 v[116:117], v72
	v_cvt_pk_f32_fp8_sdwa v[118:119], v72 src0_sel:WORD_1
	v_cvt_pk_f32_fp8_e32 v[120:121], v73
	v_cvt_pk_f32_fp8_sdwa v[122:123], v73 src0_sel:WORD_1
	v_cvt_pk_f32_fp8_e32 v[124:125], v74
	v_cvt_pk_f32_fp8_sdwa v[126:127], v74 src0_sel:WORD_1
	v_cvt_pk_f32_fp8_e32 v[128:129], v75
	v_cvt_pk_f32_fp8_sdwa v[130:131], v75 src0_sel:WORD_1
	v_lshlrev_b32_e32 v148, 16, v35
	v_mad_u32_u16 v112, v11, s46, v1
	buffer_load_dwordx4 v[72:75], v112, s[36:39], 0 offen
	v_pk_fma_f32 v[152:153], v[148:149], v[116:117], v[152:153] op_sel_hi:[0,1,1]
	v_pk_fma_f32 v[154:155], v[148:149], v[118:119], v[154:155] op_sel_hi:[0,1,1]
	v_pk_fma_f32 v[156:157], v[148:149], v[120:121], v[156:157] op_sel_hi:[0,1,1]
	v_pk_fma_f32 v[158:159], v[148:149], v[122:123], v[158:159] op_sel_hi:[0,1,1]
	v_pk_fma_f32 v[160:161], v[148:149], v[124:125], v[160:161] op_sel_hi:[0,1,1]
	v_pk_fma_f32 v[162:163], v[148:149], v[126:127], v[162:163] op_sel_hi:[0,1,1]
	v_pk_fma_f32 v[164:165], v[148:149], v[128:129], v[164:165] op_sel_hi:[0,1,1]
	v_pk_fma_f32 v[166:167], v[148:149], v[130:131], v[166:167] op_sel_hi:[0,1,1]
	s_waitcnt vmcnt(20)
	v_cvt_pk_f32_fp8_e32 v[132:133], v76
	v_cvt_pk_f32_fp8_sdwa v[134:135], v76 src0_sel:WORD_1
	v_cvt_pk_f32_fp8_e32 v[136:137], v77
	v_cvt_pk_f32_fp8_sdwa v[138:139], v77 src0_sel:WORD_1
	v_cvt_pk_f32_fp8_e32 v[140:141], v78
	v_cvt_pk_f32_fp8_sdwa v[142:143], v78 src0_sel:WORD_1
	v_cvt_pk_f32_fp8_e32 v[144:145], v79
	v_cvt_pk_f32_fp8_sdwa v[146:147], v79 src0_sel:WORD_1
	v_and_b32_e32 v150, 0xffff0000, v35
	v_mad_u32_u16 v113, v11, s46, v1 op_sel:[1,0,0,0]
	buffer_load_dwordx4 v[76:79], v113, s[36:39], 0 offen
	v_pk_fma_f32 v[152:153], v[150:151], v[132:133], v[152:153] op_sel_hi:[0,1,1]
	v_pk_fma_f32 v[154:155], v[150:151], v[134:135], v[154:155] op_sel_hi:[0,1,1]
	v_pk_fma_f32 v[156:157], v[150:151], v[136:137], v[156:157] op_sel_hi:[0,1,1]
	v_pk_fma_f32 v[158:159], v[150:151], v[138:139], v[158:159] op_sel_hi:[0,1,1]
	v_pk_fma_f32 v[160:161], v[150:151], v[140:141], v[160:161] op_sel_hi:[0,1,1]
	v_pk_fma_f32 v[162:163], v[150:151], v[142:143], v[162:163] op_sel_hi:[0,1,1]
	v_pk_fma_f32 v[164:165], v[150:151], v[144:145], v[164:165] op_sel_hi:[0,1,1]
	v_pk_fma_f32 v[166:167], v[150:151], v[146:147], v[166:167] op_sel_hi:[0,1,1]
	s_waitcnt vmcnt(20)
	v_cvt_pk_f32_fp8_e32 v[116:117], v80
	v_cvt_pk_f32_fp8_sdwa v[118:119], v80 src0_sel:WORD_1
	v_cvt_pk_f32_fp8_e32 v[120:121], v81
	v_cvt_pk_f32_fp8_sdwa v[122:123], v81 src0_sel:WORD_1
	v_cvt_pk_f32_fp8_e32 v[124:125], v82
	v_cvt_pk_f32_fp8_sdwa v[126:127], v82 src0_sel:WORD_1
	v_cvt_pk_f32_fp8_e32 v[128:129], v83
	v_cvt_pk_f32_fp8_sdwa v[130:131], v83 src0_sel:WORD_1
	v_lshlrev_b32_e32 v148, 16, v36
	v_mad_u32_u16 v112, v12, s46, v1
	buffer_load_dwordx4 v[80:83], v112, s[36:39], 0 offen
	v_pk_fma_f32 v[152:153], v[148:149], v[116:117], v[152:153] op_sel_hi:[0,1,1]
	v_pk_fma_f32 v[154:155], v[148:149], v[118:119], v[154:155] op_sel_hi:[0,1,1]
	v_pk_fma_f32 v[156:157], v[148:149], v[120:121], v[156:157] op_sel_hi:[0,1,1]
	v_pk_fma_f32 v[158:159], v[148:149], v[122:123], v[158:159] op_sel_hi:[0,1,1]
	v_pk_fma_f32 v[160:161], v[148:149], v[124:125], v[160:161] op_sel_hi:[0,1,1]
	v_pk_fma_f32 v[162:163], v[148:149], v[126:127], v[162:163] op_sel_hi:[0,1,1]
	v_pk_fma_f32 v[164:165], v[148:149], v[128:129], v[164:165] op_sel_hi:[0,1,1]
	v_pk_fma_f32 v[166:167], v[148:149], v[130:131], v[166:167] op_sel_hi:[0,1,1]
	s_waitcnt vmcnt(20)
	v_cvt_pk_f32_fp8_e32 v[132:133], v84
	v_cvt_pk_f32_fp8_sdwa v[134:135], v84 src0_sel:WORD_1
	v_cvt_pk_f32_fp8_e32 v[136:137], v85
	v_cvt_pk_f32_fp8_sdwa v[138:139], v85 src0_sel:WORD_1
	v_cvt_pk_f32_fp8_e32 v[140:141], v86
	v_cvt_pk_f32_fp8_sdwa v[142:143], v86 src0_sel:WORD_1
	v_cvt_pk_f32_fp8_e32 v[144:145], v87
	v_cvt_pk_f32_fp8_sdwa v[146:147], v87 src0_sel:WORD_1
	v_and_b32_e32 v150, 0xffff0000, v36
	v_mad_u32_u16 v113, v12, s46, v1 op_sel:[1,0,0,0]
	buffer_load_dwordx4 v[84:87], v113, s[36:39], 0 offen
	v_pk_fma_f32 v[152:153], v[150:151], v[132:133], v[152:153] op_sel_hi:[0,1,1]
	v_pk_fma_f32 v[154:155], v[150:151], v[134:135], v[154:155] op_sel_hi:[0,1,1]
	v_pk_fma_f32 v[156:157], v[150:151], v[136:137], v[156:157] op_sel_hi:[0,1,1]
	v_pk_fma_f32 v[158:159], v[150:151], v[138:139], v[158:159] op_sel_hi:[0,1,1]
	v_pk_fma_f32 v[160:161], v[150:151], v[140:141], v[160:161] op_sel_hi:[0,1,1]
	v_pk_fma_f32 v[162:163], v[150:151], v[142:143], v[162:163] op_sel_hi:[0,1,1]
	v_pk_fma_f32 v[164:165], v[150:151], v[144:145], v[164:165] op_sel_hi:[0,1,1]
	v_pk_fma_f32 v[166:167], v[150:151], v[146:147], v[166:167] op_sel_hi:[0,1,1]
	s_waitcnt vmcnt(20)
	v_cvt_pk_f32_fp8_e32 v[116:117], v88
	v_cvt_pk_f32_fp8_sdwa v[118:119], v88 src0_sel:WORD_1
	v_cvt_pk_f32_fp8_e32 v[120:121], v89
	v_cvt_pk_f32_fp8_sdwa v[122:123], v89 src0_sel:WORD_1
	v_cvt_pk_f32_fp8_e32 v[124:125], v90
	v_cvt_pk_f32_fp8_sdwa v[126:127], v90 src0_sel:WORD_1
	v_cvt_pk_f32_fp8_e32 v[128:129], v91
	v_cvt_pk_f32_fp8_sdwa v[130:131], v91 src0_sel:WORD_1
	v_lshlrev_b32_e32 v148, 16, v37
	v_mad_u32_u16 v112, v13, s46, v1
	buffer_load_dwordx4 v[88:91], v112, s[36:39], 0 offen
	v_pk_fma_f32 v[152:153], v[148:149], v[116:117], v[152:153] op_sel_hi:[0,1,1]
	v_pk_fma_f32 v[154:155], v[148:149], v[118:119], v[154:155] op_sel_hi:[0,1,1]
	v_pk_fma_f32 v[156:157], v[148:149], v[120:121], v[156:157] op_sel_hi:[0,1,1]
	v_pk_fma_f32 v[158:159], v[148:149], v[122:123], v[158:159] op_sel_hi:[0,1,1]
	v_pk_fma_f32 v[160:161], v[148:149], v[124:125], v[160:161] op_sel_hi:[0,1,1]
	v_pk_fma_f32 v[162:163], v[148:149], v[126:127], v[162:163] op_sel_hi:[0,1,1]
	v_pk_fma_f32 v[164:165], v[148:149], v[128:129], v[164:165] op_sel_hi:[0,1,1]
	v_pk_fma_f32 v[166:167], v[148:149], v[130:131], v[166:167] op_sel_hi:[0,1,1]
	s_waitcnt vmcnt(20)
	v_cvt_pk_f32_fp8_e32 v[132:133], v92
	v_cvt_pk_f32_fp8_sdwa v[134:135], v92 src0_sel:WORD_1
	v_cvt_pk_f32_fp8_e32 v[136:137], v93
	v_cvt_pk_f32_fp8_sdwa v[138:139], v93 src0_sel:WORD_1
	v_cvt_pk_f32_fp8_e32 v[140:141], v94
	v_cvt_pk_f32_fp8_sdwa v[142:143], v94 src0_sel:WORD_1
	v_cvt_pk_f32_fp8_e32 v[144:145], v95
	v_cvt_pk_f32_fp8_sdwa v[146:147], v95 src0_sel:WORD_1
	v_and_b32_e32 v150, 0xffff0000, v37
	v_mad_u32_u16 v113, v13, s46, v1 op_sel:[1,0,0,0]
	buffer_load_dwordx4 v[92:95], v113, s[36:39], 0 offen
	v_pk_fma_f32 v[152:153], v[150:151], v[132:133], v[152:153] op_sel_hi:[0,1,1]
	v_pk_fma_f32 v[154:155], v[150:151], v[134:135], v[154:155] op_sel_hi:[0,1,1]
	v_pk_fma_f32 v[156:157], v[150:151], v[136:137], v[156:157] op_sel_hi:[0,1,1]
	v_pk_fma_f32 v[158:159], v[150:151], v[138:139], v[158:159] op_sel_hi:[0,1,1]
	v_pk_fma_f32 v[160:161], v[150:151], v[140:141], v[160:161] op_sel_hi:[0,1,1]
	v_pk_fma_f32 v[162:163], v[150:151], v[142:143], v[162:163] op_sel_hi:[0,1,1]
	v_pk_fma_f32 v[164:165], v[150:151], v[144:145], v[164:165] op_sel_hi:[0,1,1]
	v_pk_fma_f32 v[166:167], v[150:151], v[146:147], v[166:167] op_sel_hi:[0,1,1]
	s_waitcnt vmcnt(20)
	v_cvt_pk_f32_fp8_e32 v[116:117], v96
	v_cvt_pk_f32_fp8_sdwa v[118:119], v96 src0_sel:WORD_1
	v_cvt_pk_f32_fp8_e32 v[120:121], v97
	v_cvt_pk_f32_fp8_sdwa v[122:123], v97 src0_sel:WORD_1
	v_cvt_pk_f32_fp8_e32 v[124:125], v98
	v_cvt_pk_f32_fp8_sdwa v[126:127], v98 src0_sel:WORD_1
	v_cvt_pk_f32_fp8_e32 v[128:129], v99
	v_cvt_pk_f32_fp8_sdwa v[130:131], v99 src0_sel:WORD_1
	v_lshlrev_b32_e32 v148, 16, v38
	v_mad_u32_u16 v112, v14, s46, v1
	buffer_load_dwordx4 v[96:99], v112, s[36:39], 0 offen
	v_pk_fma_f32 v[152:153], v[148:149], v[116:117], v[152:153] op_sel_hi:[0,1,1]
	v_pk_fma_f32 v[154:155], v[148:149], v[118:119], v[154:155] op_sel_hi:[0,1,1]
	v_pk_fma_f32 v[156:157], v[148:149], v[120:121], v[156:157] op_sel_hi:[0,1,1]
	v_pk_fma_f32 v[158:159], v[148:149], v[122:123], v[158:159] op_sel_hi:[0,1,1]
	v_pk_fma_f32 v[160:161], v[148:149], v[124:125], v[160:161] op_sel_hi:[0,1,1]
	v_pk_fma_f32 v[162:163], v[148:149], v[126:127], v[162:163] op_sel_hi:[0,1,1]
	v_pk_fma_f32 v[164:165], v[148:149], v[128:129], v[164:165] op_sel_hi:[0,1,1]
	v_pk_fma_f32 v[166:167], v[148:149], v[130:131], v[166:167] op_sel_hi:[0,1,1]
	s_waitcnt vmcnt(20)
	v_cvt_pk_f32_fp8_e32 v[132:133], v100
	v_cvt_pk_f32_fp8_sdwa v[134:135], v100 src0_sel:WORD_1
	v_cvt_pk_f32_fp8_e32 v[136:137], v101
	v_cvt_pk_f32_fp8_sdwa v[138:139], v101 src0_sel:WORD_1
	v_cvt_pk_f32_fp8_e32 v[140:141], v102
	v_cvt_pk_f32_fp8_sdwa v[142:143], v102 src0_sel:WORD_1
	v_cvt_pk_f32_fp8_e32 v[144:145], v103
	v_cvt_pk_f32_fp8_sdwa v[146:147], v103 src0_sel:WORD_1
	v_and_b32_e32 v150, 0xffff0000, v38
	v_mad_u32_u16 v113, v14, s46, v1 op_sel:[1,0,0,0]
	buffer_load_dwordx4 v[100:103], v113, s[36:39], 0 offen
	v_pk_fma_f32 v[152:153], v[150:151], v[132:133], v[152:153] op_sel_hi:[0,1,1]
	v_pk_fma_f32 v[154:155], v[150:151], v[134:135], v[154:155] op_sel_hi:[0,1,1]
	v_pk_fma_f32 v[156:157], v[150:151], v[136:137], v[156:157] op_sel_hi:[0,1,1]
	v_pk_fma_f32 v[158:159], v[150:151], v[138:139], v[158:159] op_sel_hi:[0,1,1]
	v_pk_fma_f32 v[160:161], v[150:151], v[140:141], v[160:161] op_sel_hi:[0,1,1]
	v_pk_fma_f32 v[162:163], v[150:151], v[142:143], v[162:163] op_sel_hi:[0,1,1]
	v_pk_fma_f32 v[164:165], v[150:151], v[144:145], v[164:165] op_sel_hi:[0,1,1]
	v_pk_fma_f32 v[166:167], v[150:151], v[146:147], v[166:167] op_sel_hi:[0,1,1]
	s_waitcnt vmcnt(20)
	v_cvt_pk_f32_fp8_e32 v[116:117], v104
	v_cvt_pk_f32_fp8_sdwa v[118:119], v104 src0_sel:WORD_1
	v_cvt_pk_f32_fp8_e32 v[120:121], v105
	v_cvt_pk_f32_fp8_sdwa v[122:123], v105 src0_sel:WORD_1
	v_cvt_pk_f32_fp8_e32 v[124:125], v106
	v_cvt_pk_f32_fp8_sdwa v[126:127], v106 src0_sel:WORD_1
	v_cvt_pk_f32_fp8_e32 v[128:129], v107
	v_cvt_pk_f32_fp8_sdwa v[130:131], v107 src0_sel:WORD_1
	v_lshlrev_b32_e32 v148, 16, v39
	v_mad_u32_u16 v112, v15, s46, v1
	buffer_load_dwordx4 v[104:107], v112, s[36:39], 0 offen
	v_pk_fma_f32 v[152:153], v[148:149], v[116:117], v[152:153] op_sel_hi:[0,1,1]
	v_pk_fma_f32 v[154:155], v[148:149], v[118:119], v[154:155] op_sel_hi:[0,1,1]
	v_pk_fma_f32 v[156:157], v[148:149], v[120:121], v[156:157] op_sel_hi:[0,1,1]
	v_pk_fma_f32 v[158:159], v[148:149], v[122:123], v[158:159] op_sel_hi:[0,1,1]
	v_pk_fma_f32 v[160:161], v[148:149], v[124:125], v[160:161] op_sel_hi:[0,1,1]
	v_pk_fma_f32 v[162:163], v[148:149], v[126:127], v[162:163] op_sel_hi:[0,1,1]
	v_pk_fma_f32 v[164:165], v[148:149], v[128:129], v[164:165] op_sel_hi:[0,1,1]
	v_pk_fma_f32 v[166:167], v[148:149], v[130:131], v[166:167] op_sel_hi:[0,1,1]
	s_waitcnt vmcnt(20)
	v_cvt_pk_f32_fp8_e32 v[132:133], v108
	v_cvt_pk_f32_fp8_sdwa v[134:135], v108 src0_sel:WORD_1
	v_cvt_pk_f32_fp8_e32 v[136:137], v109
	v_cvt_pk_f32_fp8_sdwa v[138:139], v109 src0_sel:WORD_1
	v_cvt_pk_f32_fp8_e32 v[140:141], v110
	v_cvt_pk_f32_fp8_sdwa v[142:143], v110 src0_sel:WORD_1
	v_cvt_pk_f32_fp8_e32 v[144:145], v111
	v_cvt_pk_f32_fp8_sdwa v[146:147], v111 src0_sel:WORD_1
	v_and_b32_e32 v150, 0xffff0000, v39
	v_mad_u32_u16 v113, v15, s46, v1 op_sel:[1,0,0,0]
	buffer_load_dwordx4 v[108:111], v113, s[36:39], 0 offen
	v_pk_fma_f32 v[152:153], v[150:151], v[132:133], v[152:153] op_sel_hi:[0,1,1]
	v_pk_fma_f32 v[154:155], v[150:151], v[134:135], v[154:155] op_sel_hi:[0,1,1]
	v_pk_fma_f32 v[156:157], v[150:151], v[136:137], v[156:157] op_sel_hi:[0,1,1]
	v_pk_fma_f32 v[158:159], v[150:151], v[138:139], v[158:159] op_sel_hi:[0,1,1]
	v_pk_fma_f32 v[160:161], v[150:151], v[140:141], v[160:161] op_sel_hi:[0,1,1]
	v_pk_fma_f32 v[162:163], v[150:151], v[142:143], v[162:163] op_sel_hi:[0,1,1]
	v_pk_fma_f32 v[164:165], v[150:151], v[144:145], v[164:165] op_sel_hi:[0,1,1]
	v_pk_fma_f32 v[166:167], v[150:151], v[146:147], v[166:167] op_sel_hi:[0,1,1]
	s_nop 1
	v_permlane32_swap_b32_e32 v152, v160
	v_permlane32_swap_b32_e32 v153, v161
	v_permlane32_swap_b32_e32 v154, v162
	v_permlane32_swap_b32_e32 v155, v163
	v_permlane32_swap_b32_e32 v156, v164
	v_permlane32_swap_b32_e32 v157, v165
	v_permlane32_swap_b32_e32 v158, v166
	v_permlane32_swap_b32_e32 v159, v167
	v_add_f32_e32 v168, v152, v160
	v_add_f32_e32 v169, v153, v161
	v_add_f32_e32 v170, v154, v162
	v_add_f32_e32 v171, v155, v163
	v_add_f32_e32 v172, v156, v164
	v_add_f32_e32 v173, v157, v165
	v_add_f32_e32 v174, v158, v166
	v_add_f32_e32 v175, v159, v167
	s_nop 1
	v_permlane16_swap_b32_e32 v168, v172
	v_permlane16_swap_b32_e32 v169, v173
	v_permlane16_swap_b32_e32 v170, v174
	v_permlane16_swap_b32_e32 v171, v175
	v_add_f32_e32 v176, v168, v172
	v_add_f32_e32 v177, v169, v173
	v_add_f32_e32 v178, v170, v174
	v_add_f32_e32 v179, v171, v175
	v_cndmask_b32_e64 v180, v176, v178, s[44:45]
	v_cndmask_b32_e64 v181, v177, v179, s[44:45]
	v_cndmask_b32_e64 v182, v178, v176, s[44:45]
	v_cndmask_b32_e64 v183, v179, v177, s[44:45]
	s_nop 0
	v_add_f32_dpp v184, v180, v182 row_ror:8 row_mask:0xf bank_mask:0xf
	v_add_f32_dpp v185, v181, v183 row_ror:8 row_mask:0xf bank_mask:0xf
	v_cvt_pk_bf16_f32 v188, v184, v185
	s_lshl_b32 s2, s20, 12
	s_add_u32 s2, s34, s2
	s_addc_u32 s3, s35, 0
	global_store_dword v3, v188, s[2:3]
	s_mov_b32 s20, s21
	s_mov_b32 s48, s49
	s_mov_b32 s21, s22
	s_mov_b32 s49, s50
	s_cmp_eq_u32 s48, 0
	s_cbranch_scc1 .Lv_drain
	s_branch .Lv_loop
